# fp8 loops now also keep 8/6 fragment reads in flight across the phase barrier with per-MFMA-pair lgkm waits (bf16 8/6 as before, reads issued first)
# baseline (speedup 1.0000x reference)
.LBB0_920:
	s_add_i32 s3, s94, 0x100
	s_add_i32 s16, s36, 0x100
	s_waitcnt lgkmcnt(8)
	s_barrier
	s_setprio 1
	v_mfma_scale_f32_16x16x128_f8f6f4 v[188:191], v[24:31], v[56:63], 0, v213, v213 op_sel_hi:[0,0,0]
	v_mfma_scale_f32_16x16x128_f8f6f4 v[184:187], v[16:23], v[56:63], 0, v213, v213 op_sel_hi:[0,0,0]
	v_mfma_scale_f32_16x16x128_f8f6f4 v[180:183], v[24:31], v[48:55], 0, v213, v213 op_sel_hi:[0,0,0]
	v_mfma_scale_f32_16x16x128_f8f6f4 v[176:179], v[16:23], v[48:55], 0, v213, v213 op_sel_hi:[0,0,0]
	s_waitcnt lgkmcnt(6)
	v_mfma_scale_f32_16x16x128_f8f6f4 v[172:175], v[24:31], v[40:47], 0, v213, v213 op_sel_hi:[0,0,0]
	v_mfma_scale_f32_16x16x128_f8f6f4 v[168:171], v[16:23], v[40:47], 0, v213, v213 op_sel_hi:[0,0,0]
	s_waitcnt lgkmcnt(4)
	v_mfma_scale_f32_16x16x128_f8f6f4 v[164:167], v[24:31], v[32:39], 0, v213, v213 op_sel_hi:[0,0,0]
	v_mfma_scale_f32_16x16x128_f8f6f4 v[160:163], v[16:23], v[32:39], 0, v213, v213 op_sel_hi:[0,0,0]
	s_setprio 0
	s_setprio 1
	s_waitcnt lgkmcnt(2)
	v_mfma_scale_f32_16x16x128_f8f6f4 v[156:159], v[8:15], v[56:63], 0, v213, v213 op_sel_hi:[0,0,0]
	s_waitcnt lgkmcnt(0)
	v_mfma_scale_f32_16x16x128_f8f6f4 v[152:155], v[0:7], v[56:63], 0, v213, v213 op_sel_hi:[0,0,0]
	v_mfma_scale_f32_16x16x128_f8f6f4 v[148:151], v[8:15], v[48:55], 0, v213, v213 op_sel_hi:[0,0,0]
	v_mfma_scale_f32_16x16x128_f8f6f4 v[144:147], v[0:7], v[48:55], 0, v213, v213 op_sel_hi:[0,0,0]
	v_mfma_scale_f32_16x16x128_f8f6f4 v[140:143], v[8:15], v[40:47], 0, v213, v213 op_sel_hi:[0,0,0]
	v_mfma_scale_f32_16x16x128_f8f6f4 v[136:139], v[0:7], v[40:47], 0, v213, v213 op_sel_hi:[0,0,0]
	v_mfma_scale_f32_16x16x128_f8f6f4 v[132:135], v[8:15], v[32:39], 0, v213, v213 op_sel_hi:[0,0,0]
	v_mfma_scale_f32_16x16x128_f8f6f4 v[128:131], v[0:7], v[32:39], 0, v213, v213 op_sel_hi:[0,0,0]
	s_setprio 0
	s_barrier
	s_mov_b32 m0, s71
	s_mov_b32 s10, s14
	s_mov_b32 s11, s15
	ds_read_b128 v[56:59], v216 offset:0x4000
	ds_read_b128 v[60:63], v216 offset:0x4400
	ds_read_b128 v[48:51], v216 offset:0x4800
	ds_read_b128 v[52:55], v216 offset:0x4c00
	ds_read_b128 v[40:43], v216 offset:0x5000
	ds_read_b128 v[44:47], v216 offset:0x5400
	ds_read_b128 v[32:35], v216 offset:0x5800
	ds_read_b128 v[36:39], v216 offset:0x5c00
	buffer_load_dwordx4 v215, s[8:11], s16 offen lds
	s_add_i32 s16, s36, 0x80100
	s_mov_b32 m0, s72
	s_and_b64 vcc, exec, s[4:5]
	buffer_load_dwordx4 v215, s[8:11], s16 offen lds
	s_add_i32 s16, s36, 0x8100
	s_mov_b32 m0, s73
	s_nop 0
	buffer_load_dwordx4 v215, s[8:11], s16 offen lds
	s_add_i32 s16, s36, 0x88100
	s_mov_b32 m0, s74
	s_nop 0
	buffer_load_dwordx4 v215, s[8:11], s16 offen lds
	s_mov_b32 m0, s70
	s_nop 0
	buffer_load_dwordx4 v214, s[12:15], s3 offen lds
	s_add_i32 s3, s94, 0x40100
	s_mov_b32 m0, s75
	s_nop 0
	buffer_load_dwordx4 v214, s[12:15], s3 offen lds
	s_cbranch_vccz .LBB0_938
	s_waitcnt vmcnt(54)
	s_cbranch_execnz .LBB0_923

.LBB0_923:
	s_add_i32 s3, s94, 0x180
	s_add_i32 s4, s36, 0x180
	s_waitcnt lgkmcnt(6)
	s_barrier
	s_setprio 1
	v_mfma_scale_f32_16x16x128_f8f6f4 v[124:127], v[24:31], v[56:63], 0, v213, v213 op_sel_hi:[0,0,0]
	v_mfma_scale_f32_16x16x128_f8f6f4 v[120:123], v[16:23], v[56:63], 0, v213, v213 op_sel_hi:[0,0,0]
	s_waitcnt lgkmcnt(4)
	v_mfma_scale_f32_16x16x128_f8f6f4 v[116:119], v[24:31], v[48:55], 0, v213, v213 op_sel_hi:[0,0,0]
	v_mfma_scale_f32_16x16x128_f8f6f4 v[112:115], v[16:23], v[48:55], 0, v213, v213 op_sel_hi:[0,0,0]
	s_waitcnt lgkmcnt(2)
	v_mfma_scale_f32_16x16x128_f8f6f4 v[108:111], v[24:31], v[40:47], 0, v213, v213 op_sel_hi:[0,0,0]
	v_mfma_scale_f32_16x16x128_f8f6f4 v[104:107], v[16:23], v[40:47], 0, v213, v213 op_sel_hi:[0,0,0]
	s_waitcnt lgkmcnt(0)
	v_mfma_scale_f32_16x16x128_f8f6f4 v[100:103], v[24:31], v[32:39], 0, v213, v213 op_sel_hi:[0,0,0]
	v_mfma_scale_f32_16x16x128_f8f6f4 v[96:99], v[16:23], v[32:39], 0, v213, v213 op_sel_hi:[0,0,0]
	s_setprio 0
	s_setprio 1
	v_mfma_scale_f32_16x16x128_f8f6f4 v[92:95], v[8:15], v[56:63], 0, v213, v213 op_sel_hi:[0,0,0]
	v_mfma_scale_f32_16x16x128_f8f6f4 v[88:91], v[0:7], v[56:63], 0, v213, v213 op_sel_hi:[0,0,0]
	v_mfma_scale_f32_16x16x128_f8f6f4 v[84:87], v[8:15], v[48:55], 0, v213, v213 op_sel_hi:[0,0,0]
	v_mfma_scale_f32_16x16x128_f8f6f4 v[80:83], v[0:7], v[48:55], 0, v213, v213 op_sel_hi:[0,0,0]
	v_mfma_scale_f32_16x16x128_f8f6f4 v[76:79], v[8:15], v[40:47], 0, v213, v213 op_sel_hi:[0,0,0]
	v_mfma_scale_f32_16x16x128_f8f6f4 v[72:75], v[0:7], v[40:47], 0, v213, v213 op_sel_hi:[0,0,0]
	v_mfma_scale_f32_16x16x128_f8f6f4 v[68:71], v[8:15], v[32:39], 0, v213, v213 op_sel_hi:[0,0,0]
	v_mfma_scale_f32_16x16x128_f8f6f4 v[64:67], v[0:7], v[32:39], 0, v213, v213 op_sel_hi:[0,0,0]
	s_setprio 0
	s_barrier
	ds_read_b128 v[24:27], v217 offset:0x8000
	ds_read_b128 v[28:31], v217 offset:0x8400
	ds_read_b128 v[16:19], v217 offset:0x8800
	ds_read_b128 v[20:23], v217 offset:0x8c00
	ds_read_b128 v[32:35], v216 offset:0x8000
	ds_read_b128 v[36:39], v216 offset:0x8400
	ds_read_b128 v[40:43], v216 offset:0x8800
	ds_read_b128 v[44:47], v216 offset:0x8c00
	ds_read_b128 v[48:51], v216 offset:0x9000
	ds_read_b128 v[52:55], v216 offset:0x9400
	ds_read_b128 v[56:59], v216 offset:0x9800
	ds_read_b128 v[60:63], v216 offset:0x9c00
	ds_read_b128 v[8:11], v217 offset:0xc000
	ds_read_b128 v[12:15], v217 offset:0xc400
	ds_read_b128 v[0:3], v217 offset:0xc800
	ds_read_b128 v[4:7], v217 offset:0xcc00
	s_mov_b32 m0, s76
	s_add_i32 s5, s94, 0x80100
	buffer_load_dwordx4 v214, s[12:15], s5 offen lds
	s_add_i32 s5, s94, 0xc0100
	s_mov_b32 m0, s77
	s_nop 0
	buffer_load_dwordx4 v214, s[12:15], s5 offen lds
	s_waitcnt vmcnt(10)
	s_waitcnt lgkmcnt(8)
	s_barrier
	s_setprio 1
	v_mfma_scale_f32_16x16x128_f8f6f4 v[188:191], v[24:31], v[32:39], v[188:191], v213, v213 op_sel_hi:[0,0,0]
	v_mfma_scale_f32_16x16x128_f8f6f4 v[184:187], v[16:23], v[32:39], v[184:187], v213, v213 op_sel_hi:[0,0,0]
	v_mfma_scale_f32_16x16x128_f8f6f4 v[180:183], v[24:31], v[40:47], v[180:183], v213, v213 op_sel_hi:[0,0,0]
	v_mfma_scale_f32_16x16x128_f8f6f4 v[176:179], v[16:23], v[40:47], v[176:179], v213, v213 op_sel_hi:[0,0,0]
	s_waitcnt lgkmcnt(6)
	v_mfma_scale_f32_16x16x128_f8f6f4 v[172:175], v[24:31], v[48:55], v[172:175], v213, v213 op_sel_hi:[0,0,0]
	v_mfma_scale_f32_16x16x128_f8f6f4 v[168:171], v[16:23], v[48:55], v[168:171], v213, v213 op_sel_hi:[0,0,0]
	s_waitcnt lgkmcnt(4)
	v_mfma_scale_f32_16x16x128_f8f6f4 v[164:167], v[24:31], v[56:63], v[164:167], v213, v213 op_sel_hi:[0,0,0]
	v_mfma_scale_f32_16x16x128_f8f6f4 v[160:163], v[16:23], v[56:63], v[160:163], v213, v213 op_sel_hi:[0,0,0]
	s_setprio 0
	s_setprio 1
	s_waitcnt lgkmcnt(2)
	v_mfma_scale_f32_16x16x128_f8f6f4 v[156:159], v[8:15], v[32:39], v[156:159], v213, v213 op_sel_hi:[0,0,0]
	s_waitcnt lgkmcnt(0)
	v_mfma_scale_f32_16x16x128_f8f6f4 v[152:155], v[0:7], v[32:39], v[152:155], v213, v213 op_sel_hi:[0,0,0]
	v_mfma_scale_f32_16x16x128_f8f6f4 v[148:151], v[8:15], v[40:47], v[148:151], v213, v213 op_sel_hi:[0,0,0]
	v_mfma_scale_f32_16x16x128_f8f6f4 v[144:147], v[0:7], v[40:47], v[144:147], v213, v213 op_sel_hi:[0,0,0]
	v_mfma_scale_f32_16x16x128_f8f6f4 v[140:143], v[8:15], v[48:55], v[140:143], v213, v213 op_sel_hi:[0,0,0]
	v_mfma_scale_f32_16x16x128_f8f6f4 v[136:139], v[0:7], v[48:55], v[136:139], v213, v213 op_sel_hi:[0,0,0]
	v_mfma_scale_f32_16x16x128_f8f6f4 v[132:135], v[8:15], v[56:63], v[132:135], v213, v213 op_sel_hi:[0,0,0]
	v_mfma_scale_f32_16x16x128_f8f6f4 v[128:131], v[0:7], v[56:63], v[128:131], v213, v213 op_sel_hi:[0,0,0]
	s_setprio 0
	s_barrier
	ds_read_b128 v[32:35], v216 offset:0xc000
	ds_read_b128 v[36:39], v216 offset:0xc400
	ds_read_b128 v[40:43], v216 offset:0xc800
	ds_read_b128 v[44:47], v216 offset:0xcc00
	ds_read_b128 v[48:51], v216 offset:0xd000
	ds_read_b128 v[52:55], v216 offset:0xd400
	ds_read_b128 v[56:59], v216 offset:0xd800
	ds_read_b128 v[60:63], v216 offset:0xdc00
	s_mov_b32 m0, s80
	s_mov_b32 s10, s14
	s_mov_b32 s11, s15
	buffer_load_dwordx4 v215, s[8:11], s4 offen lds
	s_add_i32 s4, s36, 0x80180
	s_mov_b32 m0, s81
	s_nop 0
	buffer_load_dwordx4 v215, s[8:11], s4 offen lds
	s_add_i32 s4, s36, 0x8180
	s_mov_b32 m0, s84
	s_nop 0
	buffer_load_dwordx4 v215, s[8:11], s4 offen lds
	s_add_i32 s4, s36, 0x88180
	s_mov_b32 m0, s85
	s_nop 0
	buffer_load_dwordx4 v215, s[8:11], s4 offen lds
	s_mov_b32 m0, s82
	s_nop 0
	buffer_load_dwordx4 v214, s[12:15], s3 offen lds
	s_add_i32 s3, s94, 0x40180
	s_mov_b32 m0, s83
	s_nop 0
	buffer_load_dwordx4 v214, s[12:15], s3 offen lds
	s_waitcnt vmcnt(8)
	s_waitcnt lgkmcnt(6)
	s_barrier
	s_setprio 1
	v_mfma_scale_f32_16x16x128_f8f6f4 v[124:127], v[24:31], v[32:39], v[124:127], v213, v213 op_sel_hi:[0,0,0]
	v_mfma_scale_f32_16x16x128_f8f6f4 v[120:123], v[16:23], v[32:39], v[120:123], v213, v213 op_sel_hi:[0,0,0]
	s_waitcnt lgkmcnt(4)
	v_mfma_scale_f32_16x16x128_f8f6f4 v[116:119], v[24:31], v[40:47], v[116:119], v213, v213 op_sel_hi:[0,0,0]
	v_mfma_scale_f32_16x16x128_f8f6f4 v[112:115], v[16:23], v[40:47], v[112:115], v213, v213 op_sel_hi:[0,0,0]
	s_waitcnt lgkmcnt(2)
	v_mfma_scale_f32_16x16x128_f8f6f4 v[108:111], v[24:31], v[48:55], v[108:111], v213, v213 op_sel_hi:[0,0,0]
	v_mfma_scale_f32_16x16x128_f8f6f4 v[104:107], v[16:23], v[48:55], v[104:107], v213, v213 op_sel_hi:[0,0,0]
	s_waitcnt lgkmcnt(0)
	v_mfma_scale_f32_16x16x128_f8f6f4 v[100:103], v[24:31], v[56:63], v[100:103], v213, v213 op_sel_hi:[0,0,0]
	v_mfma_scale_f32_16x16x128_f8f6f4 v[96:99], v[16:23], v[56:63], v[96:99], v213, v213 op_sel_hi:[0,0,0]
	s_setprio 0
	s_setprio 1
	v_mfma_scale_f32_16x16x128_f8f6f4 v[92:95], v[8:15], v[32:39], v[92:95], v213, v213 op_sel_hi:[0,0,0]
	v_mfma_scale_f32_16x16x128_f8f6f4 v[88:91], v[0:7], v[32:39], v[88:91], v213, v213 op_sel_hi:[0,0,0]
	v_mfma_scale_f32_16x16x128_f8f6f4 v[84:87], v[8:15], v[40:47], v[84:87], v213, v213 op_sel_hi:[0,0,0]
	v_mfma_scale_f32_16x16x128_f8f6f4 v[80:83], v[0:7], v[40:47], v[80:83], v213, v213 op_sel_hi:[0,0,0]
	v_mfma_scale_f32_16x16x128_f8f6f4 v[76:79], v[8:15], v[48:55], v[76:79], v213, v213 op_sel_hi:[0,0,0]
	v_mfma_scale_f32_16x16x128_f8f6f4 v[72:75], v[0:7], v[48:55], v[72:75], v213, v213 op_sel_hi:[0,0,0]
	v_mfma_scale_f32_16x16x128_f8f6f4 v[68:71], v[8:15], v[56:63], v[68:71], v213, v213 op_sel_hi:[0,0,0]
	v_mfma_scale_f32_16x16x128_f8f6f4 v[64:67], v[0:7], v[56:63], v[64:67], v213, v213 op_sel_hi:[0,0,0]
	s_setprio 0
	s_barrier
	s_waitcnt vmcnt(14)
	v_mul_f32_e32 v0, 0x42800000, v196
	v_mul_f32_e32 v1, 0x42800000, v192
	v_mul_f32_e32 v2, 0x42800000, v197
	v_mul_f32_e32 v3, 0x42800000, v193
	v_mul_f32_e32 v4, 0x42800000, v198
	v_mul_f32_e32 v5, 0x42800000, v194
	v_mul_f32_e32 v6, 0x42800000, v199
	v_mul_f32_e32 v7, 0x42800000, v195
	v_cvt_pk_fp8_f32 v202, v1, v0
	v_cvt_pk_fp8_f32 v219, v3, v2
	v_cvt_pk_fp8_f32 v220, v5, v4
	v_cvt_pk_fp8_f32 v221, v7, v6
	s_add_i32 s61, s36, 0x200
	s_mov_b32 s33, 0
	s_mov_b32 s79, s66
	s_mov_b32 s90, s68
	s_branch .LBB0_926

.LBB0_926:
	v_mov_b32_e32 v40, v202
	v_mov_b32_e32 v41, v219
	v_mov_b32_e32 v42, v220
	v_mov_b32_e32 v43, v221
	s_add_i32 s4, s94, s33
	s_mov_b32 s64, s90
	s_add_i32 s90, s90, 1
	s_add_i32 s3, s4, 0x200
	s_add_i32 s5, s61, s33
	ds_read_b128 v[24:27], v217 offset:0
	ds_read_b128 v[28:31], v217 offset:0x400
	ds_read_b128 v[16:19], v217 offset:0x800
	ds_read_b128 v[20:23], v217 offset:0xc00
	ds_read_b128 v[46:49], v216 offset:0
	ds_read_b128 v[50:53], v216 offset:0x400
	ds_read_b128 v[54:57], v216 offset:0x800
	ds_read_b128 v[58:61], v216 offset:0xc00
	ds_read_b128 v[192:195], v216 offset:0x1000
	ds_read_b128 v[196:199], v216 offset:0x1400
	ds_read_b128 v[220:223], v216 offset:0x1800
	ds_read_b128 v[224:227], v216 offset:0x1c00
	ds_read_b128 v[8:11], v217 offset:0x4000
	ds_read_b128 v[12:15], v217 offset:0x4400
	ds_read_b128 v[0:3], v217 offset:0x4800
	ds_read_b128 v[4:7], v217 offset:0x4c00
	s_cmpk_eq_i32 s33, 0xe00
	s_cselect_b32 s65, s60, s3
	s_cselect_b32 s16, s95, s5
	s_add_i32 s3, s65, 0x80
	s_mov_b32 m0, s86
	s_add_i32 s5, s4, 0x80180
	buffer_load_dwordx4 v214, s[12:15], s5 offen lds
	s_add_i32 s4, s4, 0xc0180
	s_mov_b32 m0, s89
	s_add_i32 s17, s16, 0x80
	buffer_load_dwordx4 v214, s[12:15], s4 offen lds
	s_lshr_b32 s4, s90, 2
	s_mul_i32 s5, s4, s34
	s_add_i32 s36, s5, s2
	s_cmp_lt_i32 s4, s47
	s_cselect_b64 s[4:5], -1, 0
	s_and_b64 s[62:63], s[4:5], exec
	s_cselect_b32 s67, s36, 0
	s_ashr_i32 s62, s67, 7
	s_bfe_u32 s36, s90, 0x10001
	s_ashr_i32 s63, s62, 31
	s_or_b32 s78, s36, s87
	s_bfe_u32 s36, s67, 0x20005
	s_lshl_b64 vcc, s[62:63], 23
	s_add_u32 vcc_lo, s28, vcc_lo
	s_addc_u32 vcc_hi, s29, vcc_hi
	s_lshl_b32 s38, s36, 21
	s_add_u32 s38, vcc_lo, s38
	s_addc_u32 s39, vcc_hi, 0
	s_lshl_b32 s67, s67, 7
	s_and_b32 s67, s67, 0xf80
	s_lshl_b32 vcc_lo, s67, 2
	s_add_u32 vcc_lo, s38, vcc_lo
	v_and_or_b32 v202, s79, 2, v200
	s_addc_u32 vcc_hi, s39, 0
	v_lshl_or_b32 v44, s78, 5, v218
	v_lshlrev_b64 v[32:33], 14, v[202:203]
	v_lshl_add_u64 v[32:33], vcc, 0, v[32:33]
	v_lshlrev_b32_e32 v202, 2, v44
	v_lshl_add_u64 v[32:33], v[32:33], 0, v[202:203]
	s_movk_i32 s38, 0x4000
	v_add_co_u32_e32 v36, vcc, s38, v32
	s_nop 1
	v_addc_co_u32_e32 v37, vcc, 0, v33, vcc
	global_load_dwordx4 v[32:35], v[32:33], off nt
	s_nop 0
	global_load_dwordx4 v[36:39], v[36:37], off nt
	s_waitcnt vmcnt(10)
	s_waitcnt lgkmcnt(8)
	s_barrier
	s_setprio 1
	v_mfma_scale_f32_16x16x128_f8f6f4 v[188:191], v[24:31], v[46:53], v[188:191], v213, v213 op_sel_hi:[0,0,0]
	v_mfma_scale_f32_16x16x128_f8f6f4 v[184:187], v[16:23], v[46:53], v[184:187], v213, v213 op_sel_hi:[0,0,0]
	v_mfma_scale_f32_16x16x128_f8f6f4 v[180:183], v[24:31], v[54:61], v[180:183], v213, v213 op_sel_hi:[0,0,0]
	v_mfma_scale_f32_16x16x128_f8f6f4 v[176:179], v[16:23], v[54:61], v[176:179], v213, v213 op_sel_hi:[0,0,0]
	s_waitcnt lgkmcnt(6)
	v_mfma_scale_f32_16x16x128_f8f6f4 v[172:175], v[24:31], v[192:199], v[172:175], v213, v213 op_sel_hi:[0,0,0]
	v_mfma_scale_f32_16x16x128_f8f6f4 v[168:171], v[16:23], v[192:199], v[168:171], v213, v213 op_sel_hi:[0,0,0]
	s_waitcnt lgkmcnt(4)
	v_mfma_scale_f32_16x16x128_f8f6f4 v[164:167], v[24:31], v[220:227], v[164:167], v213, v213 op_sel_hi:[0,0,0]
	v_mfma_scale_f32_16x16x128_f8f6f4 v[160:163], v[16:23], v[220:227], v[160:163], v213, v213 op_sel_hi:[0,0,0]
	s_setprio 0
	s_setprio 1
	s_waitcnt lgkmcnt(2)
	v_mfma_scale_f32_16x16x128_f8f6f4 v[156:159], v[8:15], v[46:53], v[156:159], v213, v213 op_sel_hi:[0,0,0]
	s_waitcnt lgkmcnt(0)
	v_mfma_scale_f32_16x16x128_f8f6f4 v[152:155], v[0:7], v[46:53], v[152:155], v213, v213 op_sel_hi:[0,0,0]
	v_mfma_scale_f32_16x16x128_f8f6f4 v[148:151], v[8:15], v[54:61], v[148:151], v213, v213 op_sel_hi:[0,0,0]
	v_mfma_scale_f32_16x16x128_f8f6f4 v[144:147], v[0:7], v[54:61], v[144:147], v213, v213 op_sel_hi:[0,0,0]
	v_mfma_scale_f32_16x16x128_f8f6f4 v[140:143], v[8:15], v[192:199], v[140:143], v213, v213 op_sel_hi:[0,0,0]
	v_mfma_scale_f32_16x16x128_f8f6f4 v[136:139], v[0:7], v[192:199], v[136:139], v213, v213 op_sel_hi:[0,0,0]
	v_mfma_scale_f32_16x16x128_f8f6f4 v[132:135], v[8:15], v[220:227], v[132:135], v213, v213 op_sel_hi:[0,0,0]
	v_mfma_scale_f32_16x16x128_f8f6f4 v[128:131], v[0:7], v[220:227], v[128:131], v213, v213 op_sel_hi:[0,0,0]
	s_setprio 0
	s_barrier
	ds_read_b128 v[46:49], v216 offset:0x4000
	ds_read_b128 v[50:53], v216 offset:0x4400
	ds_read_b128 v[54:57], v216 offset:0x4800
	ds_read_b128 v[58:61], v216 offset:0x4c00
	ds_read_b128 v[192:195], v216 offset:0x5000
	ds_read_b128 v[196:199], v216 offset:0x5400
	ds_read_b128 v[220:223], v216 offset:0x5800
	ds_read_b128 v[224:227], v216 offset:0x5c00
	s_mov_b32 m0, s71
	s_nop 0
	buffer_load_dwordx4 v215, s[8:11], s16 offen lds
	s_add_i32 s38, s16, 0x80000
	s_mov_b32 m0, s72
	s_nop 0
	buffer_load_dwordx4 v215, s[8:11], s38 offen lds
	s_add_i32 s38, s16, 0x8000
	s_mov_b32 m0, s73
	s_nop 0
	buffer_load_dwordx4 v215, s[8:11], s38 offen lds
	s_add_i32 s38, s16, 0x88000
	s_mov_b32 m0, s74
	s_nop 0
	buffer_load_dwordx4 v215, s[8:11], s38 offen lds
	s_mov_b32 m0, s70
	s_add_i32 s38, s65, 0x40000
	buffer_load_dwordx4 v214, s[12:15], s65 offen lds
	s_mov_b32 m0, s75
	s_nop 0
	buffer_load_dwordx4 v214, s[12:15], s38 offen lds
	s_waitcnt vmcnt(10)
	s_waitcnt lgkmcnt(6)
	s_barrier
	s_setprio 1
	v_mfma_scale_f32_16x16x128_f8f6f4 v[124:127], v[24:31], v[46:53], v[124:127], v213, v213 op_sel_hi:[0,0,0]
	v_mfma_scale_f32_16x16x128_f8f6f4 v[120:123], v[16:23], v[46:53], v[120:123], v213, v213 op_sel_hi:[0,0,0]
	s_waitcnt lgkmcnt(4)
	v_mfma_scale_f32_16x16x128_f8f6f4 v[116:119], v[24:31], v[54:61], v[116:119], v213, v213 op_sel_hi:[0,0,0]
	v_mfma_scale_f32_16x16x128_f8f6f4 v[112:115], v[16:23], v[54:61], v[112:115], v213, v213 op_sel_hi:[0,0,0]
	s_waitcnt lgkmcnt(2)
	v_mfma_scale_f32_16x16x128_f8f6f4 v[108:111], v[24:31], v[192:199], v[108:111], v213, v213 op_sel_hi:[0,0,0]
	v_mfma_scale_f32_16x16x128_f8f6f4 v[104:107], v[16:23], v[192:199], v[104:107], v213, v213 op_sel_hi:[0,0,0]
	s_waitcnt lgkmcnt(0)
	v_mfma_scale_f32_16x16x128_f8f6f4 v[100:103], v[24:31], v[220:227], v[100:103], v213, v213 op_sel_hi:[0,0,0]
	v_mfma_scale_f32_16x16x128_f8f6f4 v[96:99], v[16:23], v[220:227], v[96:99], v213, v213 op_sel_hi:[0,0,0]
	s_setprio 0
	s_setprio 1
	v_mfma_scale_f32_16x16x128_f8f6f4 v[92:95], v[8:15], v[46:53], v[92:95], v213, v213 op_sel_hi:[0,0,0]
	v_mfma_scale_f32_16x16x128_f8f6f4 v[88:91], v[0:7], v[46:53], v[88:91], v213, v213 op_sel_hi:[0,0,0]
	v_mfma_scale_f32_16x16x128_f8f6f4 v[84:87], v[8:15], v[54:61], v[84:87], v213, v213 op_sel_hi:[0,0,0]
	v_mfma_scale_f32_16x16x128_f8f6f4 v[80:83], v[0:7], v[54:61], v[80:83], v213, v213 op_sel_hi:[0,0,0]
	v_mfma_scale_f32_16x16x128_f8f6f4 v[76:79], v[8:15], v[192:199], v[76:79], v213, v213 op_sel_hi:[0,0,0]
	v_mfma_scale_f32_16x16x128_f8f6f4 v[72:75], v[0:7], v[192:199], v[72:75], v213, v213 op_sel_hi:[0,0,0]
	v_mfma_scale_f32_16x16x128_f8f6f4 v[68:71], v[8:15], v[220:227], v[68:71], v213, v213 op_sel_hi:[0,0,0]
	v_mfma_scale_f32_16x16x128_f8f6f4 v[64:67], v[0:7], v[220:227], v[64:67], v213, v213 op_sel_hi:[0,0,0]
	s_setprio 0
	s_barrier
	ds_read_b128 v[16:19], v217 offset:0x8000
	ds_read_b128 v[20:23], v217 offset:0x8400
	ds_read_b128 v[24:27], v217 offset:0x8800
	ds_read_b128 v[28:31], v217 offset:0x8c00
	ds_read_b128 v[46:49], v216 offset:0x8000
	ds_read_b128 v[50:53], v216 offset:0x8400
	ds_read_b128 v[54:57], v216 offset:0x8800
	ds_read_b128 v[58:61], v216 offset:0x8c00
	ds_read_b128 v[192:195], v216 offset:0x9000
	ds_read_b128 v[196:199], v216 offset:0x9400
	ds_read_b128 v[220:223], v216 offset:0x9800
	ds_read_b128 v[224:227], v216 offset:0x9c00
	ds_read_b128 v[8:11], v217 offset:0xc000
	ds_read_b128 v[12:15], v217 offset:0xc400
	ds_read_b128 v[0:3], v217 offset:0xc800
	ds_read_b128 v[4:7], v217 offset:0xcc00
	s_mov_b32 m0, s76
	s_add_i32 s38, s65, 0x80000
	buffer_load_dwordx4 v214, s[12:15], s38 offen lds
	s_add_i32 s38, s65, 0xc0000
	s_mov_b32 m0, s77
	s_nop 0
	buffer_load_dwordx4 v214, s[12:15], s38 offen lds
	s_waitcnt vmcnt(10)
	s_waitcnt lgkmcnt(8)
	s_barrier
	s_setprio 1
	v_mfma_scale_f32_16x16x128_f8f6f4 v[188:191], v[16:23], v[46:53], v[188:191], v213, v213 op_sel_hi:[0,0,0]
	v_mfma_scale_f32_16x16x128_f8f6f4 v[184:187], v[24:31], v[46:53], v[184:187], v213, v213 op_sel_hi:[0,0,0]
	v_mfma_scale_f32_16x16x128_f8f6f4 v[180:183], v[16:23], v[54:61], v[180:183], v213, v213 op_sel_hi:[0,0,0]
	v_mfma_scale_f32_16x16x128_f8f6f4 v[176:179], v[24:31], v[54:61], v[176:179], v213, v213 op_sel_hi:[0,0,0]
	s_waitcnt lgkmcnt(6)
	v_mfma_scale_f32_16x16x128_f8f6f4 v[172:175], v[16:23], v[192:199], v[172:175], v213, v213 op_sel_hi:[0,0,0]
	v_mfma_scale_f32_16x16x128_f8f6f4 v[168:171], v[24:31], v[192:199], v[168:171], v213, v213 op_sel_hi:[0,0,0]
	s_waitcnt lgkmcnt(4)
	v_mfma_scale_f32_16x16x128_f8f6f4 v[164:167], v[16:23], v[220:227], v[164:167], v213, v213 op_sel_hi:[0,0,0]
	v_mfma_scale_f32_16x16x128_f8f6f4 v[160:163], v[24:31], v[220:227], v[160:163], v213, v213 op_sel_hi:[0,0,0]
	s_setprio 0
	s_setprio 1
	s_waitcnt lgkmcnt(2)
	v_mfma_scale_f32_16x16x128_f8f6f4 v[156:159], v[8:15], v[46:53], v[156:159], v213, v213 op_sel_hi:[0,0,0]
	s_waitcnt lgkmcnt(0)
	v_mfma_scale_f32_16x16x128_f8f6f4 v[152:155], v[0:7], v[46:53], v[152:155], v213, v213 op_sel_hi:[0,0,0]
	v_mfma_scale_f32_16x16x128_f8f6f4 v[148:151], v[8:15], v[54:61], v[148:151], v213, v213 op_sel_hi:[0,0,0]
	v_mfma_scale_f32_16x16x128_f8f6f4 v[144:147], v[0:7], v[54:61], v[144:147], v213, v213 op_sel_hi:[0,0,0]
	v_mfma_scale_f32_16x16x128_f8f6f4 v[140:143], v[8:15], v[192:199], v[140:143], v213, v213 op_sel_hi:[0,0,0]
	v_mfma_scale_f32_16x16x128_f8f6f4 v[136:139], v[0:7], v[192:199], v[136:139], v213, v213 op_sel_hi:[0,0,0]
	v_mfma_scale_f32_16x16x128_f8f6f4 v[132:135], v[8:15], v[220:227], v[132:135], v213, v213 op_sel_hi:[0,0,0]
	v_mfma_scale_f32_16x16x128_f8f6f4 v[128:131], v[0:7], v[220:227], v[128:131], v213, v213 op_sel_hi:[0,0,0]
	s_setprio 0
	s_barrier
	ds_read_b128 v[46:49], v216 offset:0xc000
	ds_read_b128 v[50:53], v216 offset:0xc400
	ds_read_b128 v[54:57], v216 offset:0xc800
	ds_read_b128 v[58:61], v216 offset:0xcc00
	ds_read_b128 v[192:195], v216 offset:0xd000
	ds_read_b128 v[196:199], v216 offset:0xd400
	ds_read_b128 v[220:223], v216 offset:0xd800
	ds_read_b128 v[224:227], v216 offset:0xdc00
	s_mov_b32 m0, s80
	s_nop 0
	buffer_load_dwordx4 v215, s[8:11], s17 offen lds
	s_add_i32 s17, s16, 0x80080
	s_mov_b32 m0, s81
	s_add_i32 s65, s65, 0x40080
	buffer_load_dwordx4 v215, s[8:11], s17 offen lds
	s_add_i32 s17, s16, 0x8080
	s_mov_b32 m0, s84
	s_add_i32 s16, s16, 0x88080
	buffer_load_dwordx4 v215, s[8:11], s17 offen lds
	s_mov_b32 m0, s85
	s_nop 0
	buffer_load_dwordx4 v215, s[8:11], s16 offen lds
	s_mov_b32 m0, s82
	s_nop 0
	buffer_load_dwordx4 v214, s[12:15], s3 offen lds
	s_mov_b32 m0, s83
	s_nop 0
	buffer_load_dwordx4 v214, s[12:15], s65 offen lds
	s_waitcnt vmcnt(8)
	s_waitcnt lgkmcnt(6)
	s_barrier
	s_setprio 1
	v_mfma_scale_f32_16x16x128_f8f6f4 v[124:127], v[16:23], v[46:53], v[124:127], v213, v213 op_sel_hi:[0,0,0]
	v_mfma_scale_f32_16x16x128_f8f6f4 v[120:123], v[24:31], v[46:53], v[120:123], v213, v213 op_sel_hi:[0,0,0]
	s_waitcnt lgkmcnt(4)
	v_mfma_scale_f32_16x16x128_f8f6f4 v[116:119], v[16:23], v[54:61], v[116:119], v213, v213 op_sel_hi:[0,0,0]
	v_mfma_scale_f32_16x16x128_f8f6f4 v[112:115], v[24:31], v[54:61], v[112:115], v213, v213 op_sel_hi:[0,0,0]
	s_waitcnt lgkmcnt(2)
	v_mfma_scale_f32_16x16x128_f8f6f4 v[108:111], v[16:23], v[192:199], v[108:111], v213, v213 op_sel_hi:[0,0,0]
	v_mfma_scale_f32_16x16x128_f8f6f4 v[104:107], v[24:31], v[192:199], v[104:107], v213, v213 op_sel_hi:[0,0,0]
	s_waitcnt lgkmcnt(0)
	v_mfma_scale_f32_16x16x128_f8f6f4 v[100:103], v[16:23], v[220:227], v[100:103], v213, v213 op_sel_hi:[0,0,0]
	v_mfma_scale_f32_16x16x128_f8f6f4 v[96:99], v[24:31], v[220:227], v[96:99], v213, v213 op_sel_hi:[0,0,0]
	s_setprio 0
	s_setprio 1
	v_mfma_scale_f32_16x16x128_f8f6f4 v[92:95], v[8:15], v[46:53], v[92:95], v213, v213 op_sel_hi:[0,0,0]
	v_mfma_scale_f32_16x16x128_f8f6f4 v[88:91], v[0:7], v[46:53], v[88:91], v213, v213 op_sel_hi:[0,0,0]
	v_mfma_scale_f32_16x16x128_f8f6f4 v[84:87], v[8:15], v[54:61], v[84:87], v213, v213 op_sel_hi:[0,0,0]
	v_mfma_scale_f32_16x16x128_f8f6f4 v[80:83], v[0:7], v[54:61], v[80:83], v213, v213 op_sel_hi:[0,0,0]
	v_mfma_scale_f32_16x16x128_f8f6f4 v[76:79], v[8:15], v[192:199], v[76:79], v213, v213 op_sel_hi:[0,0,0]
	v_mfma_scale_f32_16x16x128_f8f6f4 v[72:75], v[0:7], v[192:199], v[72:75], v213, v213 op_sel_hi:[0,0,0]
	v_mfma_scale_f32_16x16x128_f8f6f4 v[68:71], v[8:15], v[220:227], v[68:71], v213, v213 op_sel_hi:[0,0,0]
	v_mfma_scale_f32_16x16x128_f8f6f4 v[64:67], v[0:7], v[220:227], v[64:67], v213, v213 op_sel_hi:[0,0,0]
	s_setprio 0
	s_barrier
	s_bitcmp0_b32 s64, 0
	s_waitcnt vmcnt(15)
	v_mul_f32_e32 v0, 0x42800000, v32
	s_waitcnt vmcnt(14)
	v_mul_f32_e32 v4, 0x42800000, v36
	v_mul_f32_e32 v1, 0x42800000, v33
	v_mul_f32_e32 v5, 0x42800000, v37
	v_mul_f32_e32 v2, 0x42800000, v34
	v_mul_f32_e32 v6, 0x42800000, v38
	v_mul_f32_e32 v3, 0x42800000, v35
	v_mul_f32_e32 v7, 0x42800000, v39
	s_mov_b64 s[64:65], -1
	s_cbranch_scc0 .LBB0_929
	s_andn2_b64 vcc, exec, s[64:65]
	s_cbranch_vccnz .LBB0_925
	s_branch .LBB0_930

.LBB0_1228:
	s_add_i32 s28, s61, 0x180
	s_add_i32 s29, s60, 0x180
	s_waitcnt lgkmcnt(6)
	s_barrier
	s_setprio 1
	v_mfma_scale_f32_16x16x128_f8f6f4 v[128:131], v[24:31], v[56:63], 0, v201, v201 op_sel_hi:[0,0,0]
	v_mfma_scale_f32_16x16x128_f8f6f4 v[124:127], v[16:23], v[56:63], 0, v201, v201 op_sel_hi:[0,0,0]
	s_waitcnt lgkmcnt(4)
	v_mfma_scale_f32_16x16x128_f8f6f4 v[120:123], v[24:31], v[48:55], 0, v201, v201 op_sel_hi:[0,0,0]
	v_mfma_scale_f32_16x16x128_f8f6f4 v[116:119], v[16:23], v[48:55], 0, v201, v201 op_sel_hi:[0,0,0]
	s_waitcnt lgkmcnt(2)
	v_mfma_scale_f32_16x16x128_f8f6f4 v[112:115], v[24:31], v[40:47], 0, v201, v201 op_sel_hi:[0,0,0]
	v_mfma_scale_f32_16x16x128_f8f6f4 v[108:111], v[16:23], v[40:47], 0, v201, v201 op_sel_hi:[0,0,0]
	s_waitcnt lgkmcnt(0)
	v_mfma_scale_f32_16x16x128_f8f6f4 v[104:107], v[24:31], v[32:39], 0, v201, v201 op_sel_hi:[0,0,0]
	v_mfma_scale_f32_16x16x128_f8f6f4 v[100:103], v[16:23], v[32:39], 0, v201, v201 op_sel_hi:[0,0,0]
	s_setprio 0
	s_setprio 1
	v_mfma_scale_f32_16x16x128_f8f6f4 v[96:99], v[8:15], v[56:63], 0, v201, v201 op_sel_hi:[0,0,0]
	v_mfma_scale_f32_16x16x128_f8f6f4 v[92:95], v[0:7], v[56:63], 0, v201, v201 op_sel_hi:[0,0,0]
	v_mfma_scale_f32_16x16x128_f8f6f4 v[88:91], v[8:15], v[48:55], 0, v201, v201 op_sel_hi:[0,0,0]
	v_mfma_scale_f32_16x16x128_f8f6f4 v[84:87], v[0:7], v[48:55], 0, v201, v201 op_sel_hi:[0,0,0]
	v_mfma_scale_f32_16x16x128_f8f6f4 v[80:83], v[8:15], v[40:47], 0, v201, v201 op_sel_hi:[0,0,0]
	v_mfma_scale_f32_16x16x128_f8f6f4 v[76:79], v[0:7], v[40:47], 0, v201, v201 op_sel_hi:[0,0,0]
	v_mfma_scale_f32_16x16x128_f8f6f4 v[72:75], v[8:15], v[32:39], 0, v201, v201 op_sel_hi:[0,0,0]
	v_mfma_scale_f32_16x16x128_f8f6f4 v[68:71], v[0:7], v[32:39], 0, v201, v201 op_sel_hi:[0,0,0]
	s_setprio 0
	s_barrier
	ds_read_b128 v[24:27], v205 offset:0x8000
	ds_read_b128 v[28:31], v205 offset:0x8400
	ds_read_b128 v[16:19], v205 offset:0x8800
	ds_read_b128 v[20:23], v205 offset:0x8c00
	ds_read_b128 v[32:35], v204 offset:0x8000
	ds_read_b128 v[36:39], v204 offset:0x8400
	ds_read_b128 v[40:43], v204 offset:0x8800
	ds_read_b128 v[44:47], v204 offset:0x8c00
	ds_read_b128 v[48:51], v204 offset:0x9000
	ds_read_b128 v[52:55], v204 offset:0x9400
	ds_read_b128 v[56:59], v204 offset:0x9800
	ds_read_b128 v[60:63], v204 offset:0x9c00
	ds_read_b128 v[8:11], v205 offset:0xc000
	ds_read_b128 v[12:15], v205 offset:0xc400
	ds_read_b128 v[0:3], v205 offset:0xc800
	ds_read_b128 v[4:7], v205 offset:0xcc00
	s_mov_b32 m0, s44
	s_nop 0
	buffer_load_dwordx4 v216, s[4:7], s33 offen lds
	s_mov_b32 m0, s45
	s_nop 0
	buffer_load_dwordx4 v215, s[4:7], s33 offen lds
	s_waitcnt vmcnt(8)
	s_waitcnt lgkmcnt(8)
	s_barrier
	s_setprio 1
	v_mfma_scale_f32_16x16x128_f8f6f4 v[192:195], v[24:31], v[32:39], v[192:195], v201, v201 op_sel_hi:[0,0,0]
	v_mfma_scale_f32_16x16x128_f8f6f4 v[188:191], v[16:23], v[32:39], v[188:191], v201, v201 op_sel_hi:[0,0,0]
	v_mfma_scale_f32_16x16x128_f8f6f4 v[184:187], v[24:31], v[40:47], v[184:187], v201, v201 op_sel_hi:[0,0,0]
	v_mfma_scale_f32_16x16x128_f8f6f4 v[180:183], v[16:23], v[40:47], v[180:183], v201, v201 op_sel_hi:[0,0,0]
	s_waitcnt lgkmcnt(6)
	v_mfma_scale_f32_16x16x128_f8f6f4 v[176:179], v[24:31], v[48:55], v[176:179], v201, v201 op_sel_hi:[0,0,0]
	v_mfma_scale_f32_16x16x128_f8f6f4 v[172:175], v[16:23], v[48:55], v[172:175], v201, v201 op_sel_hi:[0,0,0]
	s_waitcnt lgkmcnt(4)
	v_mfma_scale_f32_16x16x128_f8f6f4 v[168:171], v[24:31], v[56:63], v[168:171], v201, v201 op_sel_hi:[0,0,0]
	v_mfma_scale_f32_16x16x128_f8f6f4 v[164:167], v[16:23], v[56:63], v[164:167], v201, v201 op_sel_hi:[0,0,0]
	s_setprio 0
	s_setprio 1
	s_waitcnt lgkmcnt(2)
	v_mfma_scale_f32_16x16x128_f8f6f4 v[160:163], v[8:15], v[32:39], v[160:163], v201, v201 op_sel_hi:[0,0,0]
	s_waitcnt lgkmcnt(0)
	v_mfma_scale_f32_16x16x128_f8f6f4 v[156:159], v[0:7], v[32:39], v[156:159], v201, v201 op_sel_hi:[0,0,0]
	v_mfma_scale_f32_16x16x128_f8f6f4 v[152:155], v[8:15], v[40:47], v[152:155], v201, v201 op_sel_hi:[0,0,0]
	v_mfma_scale_f32_16x16x128_f8f6f4 v[148:151], v[0:7], v[40:47], v[148:151], v201, v201 op_sel_hi:[0,0,0]
	v_mfma_scale_f32_16x16x128_f8f6f4 v[144:147], v[8:15], v[48:55], v[144:147], v201, v201 op_sel_hi:[0,0,0]
	v_mfma_scale_f32_16x16x128_f8f6f4 v[140:143], v[0:7], v[48:55], v[140:143], v201, v201 op_sel_hi:[0,0,0]
	v_mfma_scale_f32_16x16x128_f8f6f4 v[136:139], v[8:15], v[56:63], v[136:139], v201, v201 op_sel_hi:[0,0,0]
	v_mfma_scale_f32_16x16x128_f8f6f4 v[132:135], v[0:7], v[56:63], v[132:135], v201, v201 op_sel_hi:[0,0,0]
	s_setprio 0
	s_barrier
	ds_read_b128 v[32:35], v204 offset:0xc000
	ds_read_b128 v[36:39], v204 offset:0xc400
	ds_read_b128 v[40:43], v204 offset:0xc800
	ds_read_b128 v[44:47], v204 offset:0xcc00
	ds_read_b128 v[48:51], v204 offset:0xd000
	ds_read_b128 v[52:55], v204 offset:0xd400
	ds_read_b128 v[56:59], v204 offset:0xd800
	ds_read_b128 v[60:63], v204 offset:0xdc00
	s_mov_b32 m0, s48
	s_mov_b32 s10, s6
	s_mov_b32 s11, s7
	buffer_load_dwordx4 v203, s[8:11], s29 offen lds
	s_add_i32 s29, s60, 0x80180
	s_mov_b32 m0, s49
	s_nop 0
	buffer_load_dwordx4 v203, s[8:11], s29 offen lds
	s_add_i32 s29, s60, 0x8180
	s_mov_b32 m0, s62
	s_nop 0
	buffer_load_dwordx4 v203, s[8:11], s29 offen lds
	s_add_i32 s29, s60, 0x88180
	s_mov_b32 m0, s63
	s_nop 0
	buffer_load_dwordx4 v203, s[8:11], s29 offen lds
	s_mov_b32 m0, s50
	s_nop 0
	buffer_load_dwordx4 v214, s[4:7], s28 offen lds
	s_mov_b32 m0, s51
	s_nop 0
	buffer_load_dwordx4 v217, s[4:7], s28 offen lds
	s_waitcnt vmcnt(8)
	s_waitcnt lgkmcnt(6)
	s_barrier
	s_setprio 1
	v_mfma_scale_f32_16x16x128_f8f6f4 v[128:131], v[24:31], v[32:39], v[128:131], v201, v201 op_sel_hi:[0,0,0]
	v_mfma_scale_f32_16x16x128_f8f6f4 v[124:127], v[16:23], v[32:39], v[124:127], v201, v201 op_sel_hi:[0,0,0]
	s_waitcnt lgkmcnt(4)
	v_mfma_scale_f32_16x16x128_f8f6f4 v[120:123], v[24:31], v[40:47], v[120:123], v201, v201 op_sel_hi:[0,0,0]
	v_mfma_scale_f32_16x16x128_f8f6f4 v[116:119], v[16:23], v[40:47], v[116:119], v201, v201 op_sel_hi:[0,0,0]
	s_waitcnt lgkmcnt(2)
	v_mfma_scale_f32_16x16x128_f8f6f4 v[112:115], v[24:31], v[48:55], v[112:115], v201, v201 op_sel_hi:[0,0,0]
	v_mfma_scale_f32_16x16x128_f8f6f4 v[108:111], v[16:23], v[48:55], v[108:111], v201, v201 op_sel_hi:[0,0,0]
	s_waitcnt lgkmcnt(0)
	v_mfma_scale_f32_16x16x128_f8f6f4 v[104:107], v[24:31], v[56:63], v[104:107], v201, v201 op_sel_hi:[0,0,0]
	v_mfma_scale_f32_16x16x128_f8f6f4 v[100:103], v[16:23], v[56:63], v[100:103], v201, v201 op_sel_hi:[0,0,0]
	s_setprio 0
	s_setprio 1
	v_mfma_scale_f32_16x16x128_f8f6f4 v[96:99], v[8:15], v[32:39], v[96:99], v201, v201 op_sel_hi:[0,0,0]
	v_mfma_scale_f32_16x16x128_f8f6f4 v[92:95], v[0:7], v[32:39], v[92:95], v201, v201 op_sel_hi:[0,0,0]
	v_mfma_scale_f32_16x16x128_f8f6f4 v[88:91], v[8:15], v[40:47], v[88:91], v201, v201 op_sel_hi:[0,0,0]
	v_mfma_scale_f32_16x16x128_f8f6f4 v[84:87], v[0:7], v[40:47], v[84:87], v201, v201 op_sel_hi:[0,0,0]
	v_mfma_scale_f32_16x16x128_f8f6f4 v[80:83], v[8:15], v[48:55], v[80:83], v201, v201 op_sel_hi:[0,0,0]
	v_mfma_scale_f32_16x16x128_f8f6f4 v[76:79], v[0:7], v[48:55], v[76:79], v201, v201 op_sel_hi:[0,0,0]
	v_mfma_scale_f32_16x16x128_f8f6f4 v[72:75], v[8:15], v[56:63], v[72:75], v201, v201 op_sel_hi:[0,0,0]
	v_mfma_scale_f32_16x16x128_f8f6f4 v[68:71], v[0:7], v[56:63], v[68:71], v201, v201 op_sel_hi:[0,0,0]
	s_setprio 0
	s_barrier
	s_waitcnt vmcnt(16)
	v_mbcnt_lo_u32_b32 v0, -1, 0
	v_mbcnt_hi_u32_b32 v0, -1, v0
	s_add_i32 s29, s60, 0x200
	v_lshl_add_u32 v0, v0, 4, s37
	v_ashrrev_i32_e32 v1, 31, v0
	v_lshrrev_b32_e32 v1, 22, v1
	v_add_u32_e32 v1, v0, v1
	v_ashrrev_i32_e32 v1, 10, v1
	v_mul_i32_i24_e32 v2, 0x400, v1
	v_sub_u32_e32 v2, v0, v2
	v_lshrrev_b32_e32 v3, 4, v2
	v_bitop3_b32 v3, v3, v2, 32 bitop3:0x6c
	v_ashrrev_i32_e32 v2, 31, v2
	v_lshrrev_b32_e32 v2, 26, v2
	v_add_u32_e32 v2, v3, v2
	v_and_b32_e32 v2, 0xc0, v2
	v_add_u32_e32 v0, 0x2000, v0
	v_sub_u32_e32 v2, v3, v2
	v_ashrrev_i32_e32 v3, 31, v0
	v_lshrrev_b32_e32 v3, 22, v3
	v_add_u32_e32 v3, v0, v3
	v_ashrrev_i32_e32 v3, 10, v3
	v_mul_i32_i24_e32 v4, 0x400, v3
	v_sub_u32_e32 v0, v0, v4
	v_lshrrev_b32_e32 v4, 4, v0
	v_bitop3_b32 v4, v4, v0, 32 bitop3:0x6c
	v_ashrrev_i32_e32 v0, 31, v0
	v_lshrrev_b32_e32 v0, 26, v0
	v_add_u32_e32 v0, v4, v0
	v_and_b32_e32 v0, 0xffc0, v0
	v_sub_u32_e32 v0, v4, v0
	v_lshrrev_b16_e32 v4, 7, v0
	v_and_b32_e32 v4, 1, v4
	v_add_u16_e32 v0, v0, v4
	v_lshlrev_b32_e32 v1, 5, v1
	v_ashrrev_i16_sdwa v2, v202, sext(v2) dst_sel:DWORD dst_unused:UNUSED_PAD src0_sel:DWORD src1_sel:BYTE_0
	v_lshlrev_b32_e32 v3, 5, v3
	v_ashrrev_i16_sdwa v0, v202, sext(v0) dst_sel:DWORD dst_unused:UNUSED_PAD src0_sel:DWORD src1_sel:BYTE_0
	v_and_b32_e32 v1, 32, v1
	v_bfe_i32 v2, v2, 0, 16
	v_and_b32_e32 v3, 32, v3
	v_bfe_i32 v0, v0, 0, 16
	v_add_lshl_u32 v1, v1, v2, 1
	v_add_lshl_u32 v0, v3, v0, 1
	v_lshl_add_u32 v32, v231, 12, v1
	v_lshl_add_u32 v33, v228, 12, v0
	v_lshl_add_u32 v34, v229, 12, v1
	v_lshl_add_u32 v35, v230, 12, v0
	s_mov_b32 s33, 0
.LBB0_1229:
	s_add_i32 s66, s28, 0x80
	s_cmp_eq_u32 s33, 28
	s_cselect_b64 vcc, -1, 0
	ds_read_b128 v[16:19], v205 offset:0
	ds_read_b128 v[20:23], v205 offset:0x400
	ds_read_b128 v[24:27], v205 offset:0x800
	ds_read_b128 v[28:31], v205 offset:0xc00
	ds_read_b128 v[36:39], v204 offset:0
	ds_read_b128 v[40:43], v204 offset:0x400
	ds_read_b128 v[44:47], v204 offset:0x800
	ds_read_b128 v[48:51], v204 offset:0xc00
	ds_read_b128 v[52:55], v204 offset:0x1000
	ds_read_b128 v[56:59], v204 offset:0x1400
	ds_read_b128 v[228:231], v204 offset:0x1800
	ds_read_b128 v[232:235], v204 offset:0x1c00
	ds_read_b128 v[8:11], v205 offset:0x4000
	ds_read_b128 v[12:15], v205 offset:0x4400
	ds_read_b128 v[0:3], v205 offset:0x4800
	ds_read_b128 v[4:7], v205 offset:0x4c00
	s_and_b64 s[60:61], vcc, exec
	s_cselect_b32 s66, s72, s66
	s_cselect_b32 s61, s73, s29
	s_add_i32 s60, s66, 0x80
	s_mov_b32 m0, s65
	s_nop 0
	buffer_load_dwordx4 v216, s[4:7], s28 offen lds
	s_mov_b32 m0, s68
	s_nop 0
	buffer_load_dwordx4 v215, s[4:7], s28 offen lds
	s_waitcnt vmcnt(8)
	s_waitcnt lgkmcnt(8)
	s_barrier
	s_setprio 1
	v_mfma_scale_f32_16x16x128_f8f6f4 v[192:195], v[16:23], v[36:43], v[192:195], v201, v201 op_sel_hi:[0,0,0]
	v_mfma_scale_f32_16x16x128_f8f6f4 v[188:191], v[24:31], v[36:43], v[188:191], v201, v201 op_sel_hi:[0,0,0]
	v_mfma_scale_f32_16x16x128_f8f6f4 v[184:187], v[16:23], v[44:51], v[184:187], v201, v201 op_sel_hi:[0,0,0]
	v_mfma_scale_f32_16x16x128_f8f6f4 v[180:183], v[24:31], v[44:51], v[180:183], v201, v201 op_sel_hi:[0,0,0]
	s_waitcnt lgkmcnt(6)
	v_mfma_scale_f32_16x16x128_f8f6f4 v[176:179], v[16:23], v[52:59], v[176:179], v201, v201 op_sel_hi:[0,0,0]
	v_mfma_scale_f32_16x16x128_f8f6f4 v[172:175], v[24:31], v[52:59], v[172:175], v201, v201 op_sel_hi:[0,0,0]
	s_waitcnt lgkmcnt(4)
	v_mfma_scale_f32_16x16x128_f8f6f4 v[168:171], v[16:23], v[228:235], v[168:171], v201, v201 op_sel_hi:[0,0,0]
	v_mfma_scale_f32_16x16x128_f8f6f4 v[164:167], v[24:31], v[228:235], v[164:167], v201, v201 op_sel_hi:[0,0,0]
	s_setprio 0
	s_setprio 1
	s_waitcnt lgkmcnt(2)
	v_mfma_scale_f32_16x16x128_f8f6f4 v[160:163], v[8:15], v[36:43], v[160:163], v201, v201 op_sel_hi:[0,0,0]
	s_waitcnt lgkmcnt(0)
	v_mfma_scale_f32_16x16x128_f8f6f4 v[156:159], v[0:7], v[36:43], v[156:159], v201, v201 op_sel_hi:[0,0,0]
	v_mfma_scale_f32_16x16x128_f8f6f4 v[152:155], v[8:15], v[44:51], v[152:155], v201, v201 op_sel_hi:[0,0,0]
	v_mfma_scale_f32_16x16x128_f8f6f4 v[148:151], v[0:7], v[44:51], v[148:151], v201, v201 op_sel_hi:[0,0,0]
	v_mfma_scale_f32_16x16x128_f8f6f4 v[144:147], v[8:15], v[52:59], v[144:147], v201, v201 op_sel_hi:[0,0,0]
	v_mfma_scale_f32_16x16x128_f8f6f4 v[140:143], v[0:7], v[52:59], v[140:143], v201, v201 op_sel_hi:[0,0,0]
	v_mfma_scale_f32_16x16x128_f8f6f4 v[136:139], v[8:15], v[228:235], v[136:139], v201, v201 op_sel_hi:[0,0,0]
	v_mfma_scale_f32_16x16x128_f8f6f4 v[132:135], v[0:7], v[228:235], v[132:135], v201, v201 op_sel_hi:[0,0,0]
	s_setprio 0
	s_barrier
	ds_read_b128 v[36:39], v204 offset:0x4000
	ds_read_b128 v[40:43], v204 offset:0x4400
	ds_read_b128 v[44:47], v204 offset:0x4800
	ds_read_b128 v[48:51], v204 offset:0x4c00
	ds_read_b128 v[52:55], v204 offset:0x5000
	ds_read_b128 v[56:59], v204 offset:0x5400
	ds_read_b128 v[228:231], v204 offset:0x5800
	ds_read_b128 v[232:235], v204 offset:0x5c00
	s_mov_b32 m0, s39
	s_nop 0
	buffer_load_dwordx4 v203, s[8:11], s61 offen lds
	s_add_i32 s67, s61, 0x80000
	s_mov_b32 m0, s40
	v_cndmask_b32_e32 v60, v214, v32, vcc
	buffer_load_dwordx4 v203, s[8:11], s67 offen lds
	s_add_i32 s67, s61, 0x8000
	s_mov_b32 m0, s41
	v_cndmask_b32_e32 v61, v217, v33, vcc
	buffer_load_dwordx4 v203, s[8:11], s67 offen lds
	s_add_i32 s67, s61, 0x88000
	s_mov_b32 m0, s42
	s_nop 0
	buffer_load_dwordx4 v203, s[8:11], s67 offen lds
	s_mov_b32 m0, s38
	s_nop 0
	buffer_load_dwordx4 v60, s[4:7], s66 offen lds
	s_mov_b32 m0, s43
	s_nop 0
	buffer_load_dwordx4 v61, s[4:7], s66 offen lds
	s_waitcnt vmcnt(8)
	s_waitcnt lgkmcnt(6)
	s_barrier
	s_setprio 1
	v_mfma_scale_f32_16x16x128_f8f6f4 v[128:131], v[16:23], v[36:43], v[128:131], v201, v201 op_sel_hi:[0,0,0]
	v_mfma_scale_f32_16x16x128_f8f6f4 v[124:127], v[24:31], v[36:43], v[124:127], v201, v201 op_sel_hi:[0,0,0]
	s_waitcnt lgkmcnt(4)
	v_mfma_scale_f32_16x16x128_f8f6f4 v[120:123], v[16:23], v[44:51], v[120:123], v201, v201 op_sel_hi:[0,0,0]
	v_mfma_scale_f32_16x16x128_f8f6f4 v[116:119], v[24:31], v[44:51], v[116:119], v201, v201 op_sel_hi:[0,0,0]
	s_waitcnt lgkmcnt(2)
	v_mfma_scale_f32_16x16x128_f8f6f4 v[112:115], v[16:23], v[52:59], v[112:115], v201, v201 op_sel_hi:[0,0,0]
	v_mfma_scale_f32_16x16x128_f8f6f4 v[108:111], v[24:31], v[52:59], v[108:111], v201, v201 op_sel_hi:[0,0,0]
	s_waitcnt lgkmcnt(0)
	v_mfma_scale_f32_16x16x128_f8f6f4 v[104:107], v[16:23], v[228:235], v[104:107], v201, v201 op_sel_hi:[0,0,0]
	v_mfma_scale_f32_16x16x128_f8f6f4 v[100:103], v[24:31], v[228:235], v[100:103], v201, v201 op_sel_hi:[0,0,0]
	s_setprio 0
	s_setprio 1
	v_mfma_scale_f32_16x16x128_f8f6f4 v[96:99], v[8:15], v[36:43], v[96:99], v201, v201 op_sel_hi:[0,0,0]
	v_mfma_scale_f32_16x16x128_f8f6f4 v[92:95], v[0:7], v[36:43], v[92:95], v201, v201 op_sel_hi:[0,0,0]
	v_mfma_scale_f32_16x16x128_f8f6f4 v[88:91], v[8:15], v[44:51], v[88:91], v201, v201 op_sel_hi:[0,0,0]
	v_mfma_scale_f32_16x16x128_f8f6f4 v[84:87], v[0:7], v[44:51], v[84:87], v201, v201 op_sel_hi:[0,0,0]
	v_mfma_scale_f32_16x16x128_f8f6f4 v[80:83], v[8:15], v[52:59], v[80:83], v201, v201 op_sel_hi:[0,0,0]
	v_mfma_scale_f32_16x16x128_f8f6f4 v[76:79], v[0:7], v[52:59], v[76:79], v201, v201 op_sel_hi:[0,0,0]
	v_mfma_scale_f32_16x16x128_f8f6f4 v[72:75], v[8:15], v[228:235], v[72:75], v201, v201 op_sel_hi:[0,0,0]
	v_mfma_scale_f32_16x16x128_f8f6f4 v[68:71], v[0:7], v[228:235], v[68:71], v201, v201 op_sel_hi:[0,0,0]
	s_setprio 0
	s_barrier
	ds_read_b128 v[24:27], v205 offset:0x8000
	ds_read_b128 v[28:31], v205 offset:0x8400
	ds_read_b128 v[16:19], v205 offset:0x8800
	ds_read_b128 v[20:23], v205 offset:0x8c00
	ds_read_b128 v[36:39], v204 offset:0x8000
	ds_read_b128 v[40:43], v204 offset:0x8400
	ds_read_b128 v[44:47], v204 offset:0x8800
	ds_read_b128 v[48:51], v204 offset:0x8c00
	ds_read_b128 v[52:55], v204 offset:0x9000
	ds_read_b128 v[56:59], v204 offset:0x9400
	ds_read_b128 v[228:231], v204 offset:0x9800
	ds_read_b128 v[232:235], v204 offset:0x9c00
	ds_read_b128 v[8:11], v205 offset:0xc000
	ds_read_b128 v[12:15], v205 offset:0xc400
	ds_read_b128 v[0:3], v205 offset:0xc800
	ds_read_b128 v[4:7], v205 offset:0xcc00
	s_mov_b32 m0, s44
	v_cndmask_b32_e32 v62, v216, v34, vcc
	buffer_load_dwordx4 v62, s[4:7], s66 offen lds
	v_cndmask_b32_e32 v62, v215, v35, vcc
	s_mov_b32 m0, s45
	s_nop 0
	buffer_load_dwordx4 v62, s[4:7], s66 offen lds
	s_waitcnt vmcnt(8)
	s_waitcnt lgkmcnt(8)
	s_barrier
	s_setprio 1
	v_mfma_scale_f32_16x16x128_f8f6f4 v[192:195], v[24:31], v[36:43], v[192:195], v201, v201 op_sel_hi:[0,0,0]
	v_mfma_scale_f32_16x16x128_f8f6f4 v[188:191], v[16:23], v[36:43], v[188:191], v201, v201 op_sel_hi:[0,0,0]
	v_mfma_scale_f32_16x16x128_f8f6f4 v[184:187], v[24:31], v[44:51], v[184:187], v201, v201 op_sel_hi:[0,0,0]
	v_mfma_scale_f32_16x16x128_f8f6f4 v[180:183], v[16:23], v[44:51], v[180:183], v201, v201 op_sel_hi:[0,0,0]
	s_waitcnt lgkmcnt(6)
	v_mfma_scale_f32_16x16x128_f8f6f4 v[176:179], v[24:31], v[52:59], v[176:179], v201, v201 op_sel_hi:[0,0,0]
	v_mfma_scale_f32_16x16x128_f8f6f4 v[172:175], v[16:23], v[52:59], v[172:175], v201, v201 op_sel_hi:[0,0,0]
	s_waitcnt lgkmcnt(4)
	v_mfma_scale_f32_16x16x128_f8f6f4 v[168:171], v[24:31], v[228:235], v[168:171], v201, v201 op_sel_hi:[0,0,0]
	v_mfma_scale_f32_16x16x128_f8f6f4 v[164:167], v[16:23], v[228:235], v[164:167], v201, v201 op_sel_hi:[0,0,0]
	s_setprio 0
	s_setprio 1
	s_waitcnt lgkmcnt(2)
	v_mfma_scale_f32_16x16x128_f8f6f4 v[160:163], v[8:15], v[36:43], v[160:163], v201, v201 op_sel_hi:[0,0,0]
	s_waitcnt lgkmcnt(0)
	v_mfma_scale_f32_16x16x128_f8f6f4 v[156:159], v[0:7], v[36:43], v[156:159], v201, v201 op_sel_hi:[0,0,0]
	v_mfma_scale_f32_16x16x128_f8f6f4 v[152:155], v[8:15], v[44:51], v[152:155], v201, v201 op_sel_hi:[0,0,0]
	v_mfma_scale_f32_16x16x128_f8f6f4 v[148:151], v[0:7], v[44:51], v[148:151], v201, v201 op_sel_hi:[0,0,0]
	v_mfma_scale_f32_16x16x128_f8f6f4 v[144:147], v[8:15], v[52:59], v[144:147], v201, v201 op_sel_hi:[0,0,0]
	v_mfma_scale_f32_16x16x128_f8f6f4 v[140:143], v[0:7], v[52:59], v[140:143], v201, v201 op_sel_hi:[0,0,0]
	v_mfma_scale_f32_16x16x128_f8f6f4 v[136:139], v[8:15], v[228:235], v[136:139], v201, v201 op_sel_hi:[0,0,0]
	v_mfma_scale_f32_16x16x128_f8f6f4 v[132:135], v[0:7], v[228:235], v[132:135], v201, v201 op_sel_hi:[0,0,0]
	s_setprio 0
	s_barrier
	ds_read_b128 v[36:39], v204 offset:0xc000
	ds_read_b128 v[40:43], v204 offset:0xc400
	ds_read_b128 v[44:47], v204 offset:0xc800
	ds_read_b128 v[48:51], v204 offset:0xcc00
	ds_read_b128 v[52:55], v204 offset:0xd000
	ds_read_b128 v[56:59], v204 offset:0xd400
	ds_read_b128 v[228:231], v204 offset:0xd800
	ds_read_b128 v[232:235], v204 offset:0xdc00
	s_mov_b32 m0, s48
	s_add_i32 s66, s61, 0x80
	buffer_load_dwordx4 v203, s[8:11], s66 offen lds
	s_add_i32 s66, s61, 0x80080
	s_mov_b32 m0, s49
	s_nop 0
	buffer_load_dwordx4 v203, s[8:11], s66 offen lds
	s_add_i32 s66, s61, 0x8080
	s_mov_b32 m0, s62
	s_add_i32 s61, s61, 0x88080
	buffer_load_dwordx4 v203, s[8:11], s66 offen lds
	s_mov_b32 m0, s63
	s_nop 0
	buffer_load_dwordx4 v203, s[8:11], s61 offen lds
	s_mov_b32 m0, s50
	s_nop 0
	buffer_load_dwordx4 v60, s[4:7], s60 offen lds
	s_mov_b32 m0, s51
	s_nop 0
	buffer_load_dwordx4 v61, s[4:7], s60 offen lds
	s_waitcnt vmcnt(8)
	s_waitcnt lgkmcnt(6)
	s_barrier
	s_setprio 1
	v_mfma_scale_f32_16x16x128_f8f6f4 v[128:131], v[24:31], v[36:43], v[128:131], v201, v201 op_sel_hi:[0,0,0]
	v_mfma_scale_f32_16x16x128_f8f6f4 v[124:127], v[16:23], v[36:43], v[124:127], v201, v201 op_sel_hi:[0,0,0]
	s_waitcnt lgkmcnt(4)
	v_mfma_scale_f32_16x16x128_f8f6f4 v[120:123], v[24:31], v[44:51], v[120:123], v201, v201 op_sel_hi:[0,0,0]
	v_mfma_scale_f32_16x16x128_f8f6f4 v[116:119], v[16:23], v[44:51], v[116:119], v201, v201 op_sel_hi:[0,0,0]
	s_waitcnt lgkmcnt(2)
	v_mfma_scale_f32_16x16x128_f8f6f4 v[112:115], v[24:31], v[52:59], v[112:115], v201, v201 op_sel_hi:[0,0,0]
	v_mfma_scale_f32_16x16x128_f8f6f4 v[108:111], v[16:23], v[52:59], v[108:111], v201, v201 op_sel_hi:[0,0,0]
	s_waitcnt lgkmcnt(0)
	v_mfma_scale_f32_16x16x128_f8f6f4 v[104:107], v[24:31], v[228:235], v[104:107], v201, v201 op_sel_hi:[0,0,0]
	v_mfma_scale_f32_16x16x128_f8f6f4 v[100:103], v[16:23], v[228:235], v[100:103], v201, v201 op_sel_hi:[0,0,0]
	s_setprio 0
	s_setprio 1
	v_mfma_scale_f32_16x16x128_f8f6f4 v[96:99], v[8:15], v[36:43], v[96:99], v201, v201 op_sel_hi:[0,0,0]
	v_mfma_scale_f32_16x16x128_f8f6f4 v[92:95], v[0:7], v[36:43], v[92:95], v201, v201 op_sel_hi:[0,0,0]
	v_mfma_scale_f32_16x16x128_f8f6f4 v[88:91], v[8:15], v[44:51], v[88:91], v201, v201 op_sel_hi:[0,0,0]
	v_mfma_scale_f32_16x16x128_f8f6f4 v[84:87], v[0:7], v[44:51], v[84:87], v201, v201 op_sel_hi:[0,0,0]
	v_mfma_scale_f32_16x16x128_f8f6f4 v[80:83], v[8:15], v[52:59], v[80:83], v201, v201 op_sel_hi:[0,0,0]
	v_mfma_scale_f32_16x16x128_f8f6f4 v[76:79], v[0:7], v[52:59], v[76:79], v201, v201 op_sel_hi:[0,0,0]
	v_mfma_scale_f32_16x16x128_f8f6f4 v[72:75], v[8:15], v[228:235], v[72:75], v201, v201 op_sel_hi:[0,0,0]
	v_mfma_scale_f32_16x16x128_f8f6f4 v[68:71], v[0:7], v[228:235], v[68:71], v201, v201 op_sel_hi:[0,0,0]
	s_setprio 0
	s_barrier
	s_add_i32 s33, s33, 2
	s_addk_i32 s28, 0x100
	s_addk_i32 s29, 0x100
	s_cmp_gt_u32 s33, 29
	s_cbranch_scc0 .LBB0_1229
	s_and_b64 vcc, exec, s[18:19]
	s_cbranch_vccz .LBB0_1232
	s_barrier

.LBB0_1329:
	s_add_i32 s36, s89, 0x180
	s_add_i32 s37, s61, 0x180
	s_waitcnt lgkmcnt(6)
	s_barrier
	s_setprio 1
	v_mfma_scale_f32_16x16x128_f8f6f4 v[128:131], v[24:31], v[56:63], 0, v198, v198 op_sel_hi:[0,0,0]
	v_mfma_scale_f32_16x16x128_f8f6f4 v[124:127], v[16:23], v[56:63], 0, v198, v198 op_sel_hi:[0,0,0]
	s_waitcnt lgkmcnt(4)
	v_mfma_scale_f32_16x16x128_f8f6f4 v[120:123], v[24:31], v[48:55], 0, v198, v198 op_sel_hi:[0,0,0]
	v_mfma_scale_f32_16x16x128_f8f6f4 v[116:119], v[16:23], v[48:55], 0, v198, v198 op_sel_hi:[0,0,0]
	s_waitcnt lgkmcnt(2)
	v_mfma_scale_f32_16x16x128_f8f6f4 v[112:115], v[24:31], v[40:47], 0, v198, v198 op_sel_hi:[0,0,0]
	v_mfma_scale_f32_16x16x128_f8f6f4 v[108:111], v[16:23], v[40:47], 0, v198, v198 op_sel_hi:[0,0,0]
	s_waitcnt lgkmcnt(0)
	v_mfma_scale_f32_16x16x128_f8f6f4 v[104:107], v[24:31], v[32:39], 0, v198, v198 op_sel_hi:[0,0,0]
	v_mfma_scale_f32_16x16x128_f8f6f4 v[100:103], v[16:23], v[32:39], 0, v198, v198 op_sel_hi:[0,0,0]
	s_setprio 0
	s_setprio 1
	v_mfma_scale_f32_16x16x128_f8f6f4 v[96:99], v[8:15], v[56:63], 0, v198, v198 op_sel_hi:[0,0,0]
	v_mfma_scale_f32_16x16x128_f8f6f4 v[92:95], v[0:7], v[56:63], 0, v198, v198 op_sel_hi:[0,0,0]
	v_mfma_scale_f32_16x16x128_f8f6f4 v[88:91], v[8:15], v[48:55], 0, v198, v198 op_sel_hi:[0,0,0]
	v_mfma_scale_f32_16x16x128_f8f6f4 v[84:87], v[0:7], v[48:55], 0, v198, v198 op_sel_hi:[0,0,0]
	v_mfma_scale_f32_16x16x128_f8f6f4 v[80:83], v[8:15], v[40:47], 0, v198, v198 op_sel_hi:[0,0,0]
	v_mfma_scale_f32_16x16x128_f8f6f4 v[76:79], v[0:7], v[40:47], 0, v198, v198 op_sel_hi:[0,0,0]
	v_mfma_scale_f32_16x16x128_f8f6f4 v[72:75], v[8:15], v[32:39], 0, v198, v198 op_sel_hi:[0,0,0]
	v_mfma_scale_f32_16x16x128_f8f6f4 v[68:71], v[0:7], v[32:39], 0, v198, v198 op_sel_hi:[0,0,0]
	s_setprio 0
	s_barrier
	ds_read_b128 v[24:27], v202 offset:0x8000
	ds_read_b128 v[28:31], v202 offset:0x8400
	ds_read_b128 v[16:19], v202 offset:0x8800
	ds_read_b128 v[20:23], v202 offset:0x8c00
	ds_read_b128 v[32:35], v201 offset:0x8000
	ds_read_b128 v[36:39], v201 offset:0x8400
	ds_read_b128 v[40:43], v201 offset:0x8800
	ds_read_b128 v[44:47], v201 offset:0x8c00
	ds_read_b128 v[48:51], v201 offset:0x9000
	ds_read_b128 v[52:55], v201 offset:0x9400
	ds_read_b128 v[56:59], v201 offset:0x9800
	ds_read_b128 v[60:63], v201 offset:0x9c00
	ds_read_b128 v[8:11], v202 offset:0xc000
	ds_read_b128 v[12:15], v202 offset:0xc400
	ds_read_b128 v[0:3], v202 offset:0xc800
	ds_read_b128 v[4:7], v202 offset:0xcc00
	s_mov_b32 m0, s50
	s_nop 0
	buffer_load_dwordx4 v207, s[4:7], s33 offen lds
	s_mov_b32 m0, s51
	s_nop 0
	buffer_load_dwordx4 v206, s[4:7], s33 offen lds
	s_waitcnt vmcnt(8)
	s_waitcnt lgkmcnt(8)
	s_barrier
	s_setprio 1
	v_mfma_scale_f32_16x16x128_f8f6f4 v[192:195], v[24:31], v[32:39], v[192:195], v198, v198 op_sel_hi:[0,0,0]
	v_mfma_scale_f32_16x16x128_f8f6f4 v[188:191], v[16:23], v[32:39], v[188:191], v198, v198 op_sel_hi:[0,0,0]
	v_mfma_scale_f32_16x16x128_f8f6f4 v[184:187], v[24:31], v[40:47], v[184:187], v198, v198 op_sel_hi:[0,0,0]
	v_mfma_scale_f32_16x16x128_f8f6f4 v[180:183], v[16:23], v[40:47], v[180:183], v198, v198 op_sel_hi:[0,0,0]
	s_waitcnt lgkmcnt(6)
	v_mfma_scale_f32_16x16x128_f8f6f4 v[176:179], v[24:31], v[48:55], v[176:179], v198, v198 op_sel_hi:[0,0,0]
	v_mfma_scale_f32_16x16x128_f8f6f4 v[172:175], v[16:23], v[48:55], v[172:175], v198, v198 op_sel_hi:[0,0,0]
	s_waitcnt lgkmcnt(4)
	v_mfma_scale_f32_16x16x128_f8f6f4 v[168:171], v[24:31], v[56:63], v[168:171], v198, v198 op_sel_hi:[0,0,0]
	v_mfma_scale_f32_16x16x128_f8f6f4 v[164:167], v[16:23], v[56:63], v[164:167], v198, v198 op_sel_hi:[0,0,0]
	s_setprio 0
	s_setprio 1
	s_waitcnt lgkmcnt(2)
	v_mfma_scale_f32_16x16x128_f8f6f4 v[160:163], v[8:15], v[32:39], v[160:163], v198, v198 op_sel_hi:[0,0,0]
	s_waitcnt lgkmcnt(0)
	v_mfma_scale_f32_16x16x128_f8f6f4 v[156:159], v[0:7], v[32:39], v[156:159], v198, v198 op_sel_hi:[0,0,0]
	v_mfma_scale_f32_16x16x128_f8f6f4 v[152:155], v[8:15], v[40:47], v[152:155], v198, v198 op_sel_hi:[0,0,0]
	v_mfma_scale_f32_16x16x128_f8f6f4 v[148:151], v[0:7], v[40:47], v[148:151], v198, v198 op_sel_hi:[0,0,0]
	v_mfma_scale_f32_16x16x128_f8f6f4 v[144:147], v[8:15], v[48:55], v[144:147], v198, v198 op_sel_hi:[0,0,0]
	v_mfma_scale_f32_16x16x128_f8f6f4 v[140:143], v[0:7], v[48:55], v[140:143], v198, v198 op_sel_hi:[0,0,0]
	v_mfma_scale_f32_16x16x128_f8f6f4 v[136:139], v[8:15], v[56:63], v[136:139], v198, v198 op_sel_hi:[0,0,0]
	v_mfma_scale_f32_16x16x128_f8f6f4 v[132:135], v[0:7], v[56:63], v[132:135], v198, v198 op_sel_hi:[0,0,0]
	s_setprio 0
	s_barrier
	ds_read_b128 v[32:35], v201 offset:0xc000
	ds_read_b128 v[36:39], v201 offset:0xc400
	ds_read_b128 v[40:43], v201 offset:0xc800
	ds_read_b128 v[44:47], v201 offset:0xcc00
	ds_read_b128 v[48:51], v201 offset:0xd000
	ds_read_b128 v[52:55], v201 offset:0xd400
	ds_read_b128 v[56:59], v201 offset:0xd800
	ds_read_b128 v[60:63], v201 offset:0xdc00
	s_mov_b32 m0, s64
	s_mov_b32 s10, s6
	s_mov_b32 s11, s7
	buffer_load_dwordx4 v200, s[8:11], s37 offen lds
	s_add_i32 s33, s61, 0x80180
	s_mov_b32 m0, s65
	s_nop 0
	buffer_load_dwordx4 v200, s[8:11], s33 offen lds
	s_add_i32 s33, s61, 0x8180
	s_mov_b32 m0, s70
	s_nop 0
	buffer_load_dwordx4 v200, s[8:11], s33 offen lds
	s_add_i32 s33, s61, 0x88180
	s_mov_b32 m0, s71
	s_nop 0
	buffer_load_dwordx4 v200, s[8:11], s33 offen lds
	s_mov_b32 m0, s68
	s_nop 0
	buffer_load_dwordx4 v205, s[4:7], s36 offen lds
	s_mov_b32 m0, s69
	s_nop 0
	buffer_load_dwordx4 v208, s[4:7], s36 offen lds
	s_waitcnt vmcnt(8)
	s_waitcnt lgkmcnt(6)
	s_barrier
	s_setprio 1
	v_mfma_scale_f32_16x16x128_f8f6f4 v[128:131], v[24:31], v[32:39], v[128:131], v198, v198 op_sel_hi:[0,0,0]
	v_mfma_scale_f32_16x16x128_f8f6f4 v[124:127], v[16:23], v[32:39], v[124:127], v198, v198 op_sel_hi:[0,0,0]
	s_waitcnt lgkmcnt(4)
	v_mfma_scale_f32_16x16x128_f8f6f4 v[120:123], v[24:31], v[40:47], v[120:123], v198, v198 op_sel_hi:[0,0,0]
	v_mfma_scale_f32_16x16x128_f8f6f4 v[116:119], v[16:23], v[40:47], v[116:119], v198, v198 op_sel_hi:[0,0,0]
	s_waitcnt lgkmcnt(2)
	v_mfma_scale_f32_16x16x128_f8f6f4 v[112:115], v[24:31], v[48:55], v[112:115], v198, v198 op_sel_hi:[0,0,0]
	v_mfma_scale_f32_16x16x128_f8f6f4 v[108:111], v[16:23], v[48:55], v[108:111], v198, v198 op_sel_hi:[0,0,0]
	s_waitcnt lgkmcnt(0)
	v_mfma_scale_f32_16x16x128_f8f6f4 v[104:107], v[24:31], v[56:63], v[104:107], v198, v198 op_sel_hi:[0,0,0]
	v_mfma_scale_f32_16x16x128_f8f6f4 v[100:103], v[16:23], v[56:63], v[100:103], v198, v198 op_sel_hi:[0,0,0]
	s_setprio 0
	s_setprio 1
	v_mfma_scale_f32_16x16x128_f8f6f4 v[96:99], v[8:15], v[32:39], v[96:99], v198, v198 op_sel_hi:[0,0,0]
	v_mfma_scale_f32_16x16x128_f8f6f4 v[92:95], v[0:7], v[32:39], v[92:95], v198, v198 op_sel_hi:[0,0,0]
	v_mfma_scale_f32_16x16x128_f8f6f4 v[88:91], v[8:15], v[40:47], v[88:91], v198, v198 op_sel_hi:[0,0,0]
	v_mfma_scale_f32_16x16x128_f8f6f4 v[84:87], v[0:7], v[40:47], v[84:87], v198, v198 op_sel_hi:[0,0,0]
	v_mfma_scale_f32_16x16x128_f8f6f4 v[80:83], v[8:15], v[48:55], v[80:83], v198, v198 op_sel_hi:[0,0,0]
	v_mfma_scale_f32_16x16x128_f8f6f4 v[76:79], v[0:7], v[48:55], v[76:79], v198, v198 op_sel_hi:[0,0,0]
	v_mfma_scale_f32_16x16x128_f8f6f4 v[72:75], v[8:15], v[56:63], v[72:75], v198, v198 op_sel_hi:[0,0,0]
	v_mfma_scale_f32_16x16x128_f8f6f4 v[68:71], v[0:7], v[56:63], v[68:71], v198, v198 op_sel_hi:[0,0,0]
	s_setprio 0
	s_barrier
	s_waitcnt vmcnt(16)
	v_mbcnt_lo_u32_b32 v0, -1, 0
	v_mbcnt_hi_u32_b32 v0, -1, v0
	s_add_i32 s33, s61, 0x200
	v_lshl_add_u32 v0, v0, 4, s40
	v_ashrrev_i32_e32 v1, 31, v0
	v_lshrrev_b32_e32 v1, 22, v1
	v_add_u32_e32 v1, v0, v1
	v_ashrrev_i32_e32 v1, 10, v1
	v_mul_i32_i24_e32 v2, 0x400, v1
	v_sub_u32_e32 v2, v0, v2
	v_lshrrev_b32_e32 v3, 4, v2
	v_bitop3_b32 v3, v3, v2, 32 bitop3:0x6c
	v_ashrrev_i32_e32 v2, 31, v2
	v_lshrrev_b32_e32 v2, 26, v2
	v_add_u32_e32 v2, v3, v2
	v_and_b32_e32 v2, 0xc0, v2
	v_add_u32_e32 v0, 0x2000, v0
	v_sub_u32_e32 v2, v3, v2
	v_ashrrev_i32_e32 v3, 31, v0
	v_lshrrev_b32_e32 v3, 22, v3
	v_add_u32_e32 v3, v0, v3
	v_ashrrev_i32_e32 v3, 10, v3
	v_mul_i32_i24_e32 v4, 0x400, v3
	v_sub_u32_e32 v0, v0, v4
	v_lshrrev_b32_e32 v4, 4, v0
	v_bitop3_b32 v4, v4, v0, 32 bitop3:0x6c
	v_ashrrev_i32_e32 v0, 31, v0
	v_lshrrev_b32_e32 v0, 26, v0
	v_add_u32_e32 v0, v4, v0
	v_and_b32_e32 v0, 0xffc0, v0
	v_sub_u32_e32 v0, v4, v0
	v_lshrrev_b16_e32 v4, 7, v0
	v_and_b32_e32 v4, 1, v4
	v_add_u16_e32 v0, v0, v4
	v_lshlrev_b32_e32 v1, 5, v1
	v_ashrrev_i16_sdwa v2, v199, sext(v2) dst_sel:DWORD dst_unused:UNUSED_PAD src0_sel:DWORD src1_sel:BYTE_0
	v_lshlrev_b32_e32 v3, 5, v3
	v_ashrrev_i16_sdwa v0, v199, sext(v0) dst_sel:DWORD dst_unused:UNUSED_PAD src0_sel:DWORD src1_sel:BYTE_0
	v_and_b32_e32 v1, 32, v1
	v_bfe_i32 v2, v2, 0, 16
	v_and_b32_e32 v3, 32, v3
	v_bfe_i32 v0, v0, 0, 16
	v_add_lshl_u32 v1, v1, v2, 1
	v_add_lshl_u32 v0, v3, v0, 1
	v_lshl_add_u32 v32, v220, 12, v1
	v_lshl_add_u32 v33, v217, 12, v0
	v_lshl_add_u32 v34, v218, 12, v1
	v_lshl_add_u32 v35, v219, 12, v0
	s_mov_b32 s37, 0
.LBB0_1330:
	s_add_i32 s61, s36, 0x80
	s_cmp_eq_u32 s37, 28
	s_cselect_b64 vcc, -1, 0
	ds_read_b128 v[16:19], v202 offset:0
	ds_read_b128 v[20:23], v202 offset:0x400
	ds_read_b128 v[24:27], v202 offset:0x800
	ds_read_b128 v[28:31], v202 offset:0xc00
	ds_read_b128 v[36:39], v201 offset:0
	ds_read_b128 v[40:43], v201 offset:0x400
	ds_read_b128 v[44:47], v201 offset:0x800
	ds_read_b128 v[48:51], v201 offset:0xc00
	ds_read_b128 v[52:55], v201 offset:0x1000
	ds_read_b128 v[56:59], v201 offset:0x1400
	ds_read_b128 v[218:221], v201 offset:0x1800
	ds_read_b128 v[222:225], v201 offset:0x1c00
	ds_read_b128 v[8:11], v202 offset:0x4000
	ds_read_b128 v[12:15], v202 offset:0x4400
	ds_read_b128 v[0:3], v202 offset:0x4800
	ds_read_b128 v[4:7], v202 offset:0x4c00
	s_and_b64 s[66:67], vcc, exec
	s_cselect_b32 s67, s85, s61
	s_cselect_b32 s66, s86, s33
	s_add_i32 s61, s67, 0x80
	s_mov_b32 m0, s73
	s_nop 0
	buffer_load_dwordx4 v207, s[4:7], s36 offen lds
	s_mov_b32 m0, s74
	s_nop 0
	buffer_load_dwordx4 v206, s[4:7], s36 offen lds
	s_waitcnt vmcnt(8)
	s_waitcnt lgkmcnt(8)
	s_barrier
	s_setprio 1
	v_mfma_scale_f32_16x16x128_f8f6f4 v[192:195], v[16:23], v[36:43], v[192:195], v198, v198 op_sel_hi:[0,0,0]
	v_mfma_scale_f32_16x16x128_f8f6f4 v[188:191], v[24:31], v[36:43], v[188:191], v198, v198 op_sel_hi:[0,0,0]
	v_mfma_scale_f32_16x16x128_f8f6f4 v[184:187], v[16:23], v[44:51], v[184:187], v198, v198 op_sel_hi:[0,0,0]
	v_mfma_scale_f32_16x16x128_f8f6f4 v[180:183], v[24:31], v[44:51], v[180:183], v198, v198 op_sel_hi:[0,0,0]
	s_waitcnt lgkmcnt(6)
	v_mfma_scale_f32_16x16x128_f8f6f4 v[176:179], v[16:23], v[52:59], v[176:179], v198, v198 op_sel_hi:[0,0,0]
	v_mfma_scale_f32_16x16x128_f8f6f4 v[172:175], v[24:31], v[52:59], v[172:175], v198, v198 op_sel_hi:[0,0,0]
	s_waitcnt lgkmcnt(4)
	v_mfma_scale_f32_16x16x128_f8f6f4 v[168:171], v[16:23], v[218:225], v[168:171], v198, v198 op_sel_hi:[0,0,0]
	v_mfma_scale_f32_16x16x128_f8f6f4 v[164:167], v[24:31], v[218:225], v[164:167], v198, v198 op_sel_hi:[0,0,0]
	s_setprio 0
	s_setprio 1
	s_waitcnt lgkmcnt(2)
	v_mfma_scale_f32_16x16x128_f8f6f4 v[160:163], v[8:15], v[36:43], v[160:163], v198, v198 op_sel_hi:[0,0,0]
	s_waitcnt lgkmcnt(0)
	v_mfma_scale_f32_16x16x128_f8f6f4 v[156:159], v[0:7], v[36:43], v[156:159], v198, v198 op_sel_hi:[0,0,0]
	v_mfma_scale_f32_16x16x128_f8f6f4 v[152:155], v[8:15], v[44:51], v[152:155], v198, v198 op_sel_hi:[0,0,0]
	v_mfma_scale_f32_16x16x128_f8f6f4 v[148:151], v[0:7], v[44:51], v[148:151], v198, v198 op_sel_hi:[0,0,0]
	v_mfma_scale_f32_16x16x128_f8f6f4 v[144:147], v[8:15], v[52:59], v[144:147], v198, v198 op_sel_hi:[0,0,0]
	v_mfma_scale_f32_16x16x128_f8f6f4 v[140:143], v[0:7], v[52:59], v[140:143], v198, v198 op_sel_hi:[0,0,0]
	v_mfma_scale_f32_16x16x128_f8f6f4 v[136:139], v[8:15], v[218:225], v[136:139], v198, v198 op_sel_hi:[0,0,0]
	v_mfma_scale_f32_16x16x128_f8f6f4 v[132:135], v[0:7], v[218:225], v[132:135], v198, v198 op_sel_hi:[0,0,0]
	s_setprio 0
	s_barrier
	ds_read_b128 v[36:39], v201 offset:0x4000
	ds_read_b128 v[40:43], v201 offset:0x4400
	ds_read_b128 v[44:47], v201 offset:0x4800
	ds_read_b128 v[48:51], v201 offset:0x4c00
	ds_read_b128 v[52:55], v201 offset:0x5000
	ds_read_b128 v[56:59], v201 offset:0x5400
	ds_read_b128 v[218:221], v201 offset:0x5800
	ds_read_b128 v[222:225], v201 offset:0x5c00
	s_mov_b32 m0, s45
	s_nop 0
	buffer_load_dwordx4 v200, s[8:11], s66 offen lds
	s_add_i32 s89, s66, 0x80000
	s_mov_b32 m0, s46
	v_cndmask_b32_e32 v60, v205, v32, vcc
	buffer_load_dwordx4 v200, s[8:11], s89 offen lds
	s_add_i32 s89, s66, 0x8000
	s_mov_b32 m0, s47
	v_cndmask_b32_e32 v61, v208, v33, vcc
	buffer_load_dwordx4 v200, s[8:11], s89 offen lds
	s_add_i32 s89, s66, 0x88000
	s_mov_b32 m0, s48
	s_nop 0
	buffer_load_dwordx4 v200, s[8:11], s89 offen lds
	s_mov_b32 m0, s44
	s_nop 0
	buffer_load_dwordx4 v60, s[4:7], s67 offen lds
	s_mov_b32 m0, s49
	s_nop 0
	buffer_load_dwordx4 v61, s[4:7], s67 offen lds
	s_waitcnt vmcnt(8)
	s_waitcnt lgkmcnt(6)
	s_barrier
	s_setprio 1
	v_mfma_scale_f32_16x16x128_f8f6f4 v[128:131], v[16:23], v[36:43], v[128:131], v198, v198 op_sel_hi:[0,0,0]
	v_mfma_scale_f32_16x16x128_f8f6f4 v[124:127], v[24:31], v[36:43], v[124:127], v198, v198 op_sel_hi:[0,0,0]
	s_waitcnt lgkmcnt(4)
	v_mfma_scale_f32_16x16x128_f8f6f4 v[120:123], v[16:23], v[44:51], v[120:123], v198, v198 op_sel_hi:[0,0,0]
	v_mfma_scale_f32_16x16x128_f8f6f4 v[116:119], v[24:31], v[44:51], v[116:119], v198, v198 op_sel_hi:[0,0,0]
	s_waitcnt lgkmcnt(2)
	v_mfma_scale_f32_16x16x128_f8f6f4 v[112:115], v[16:23], v[52:59], v[112:115], v198, v198 op_sel_hi:[0,0,0]
	v_mfma_scale_f32_16x16x128_f8f6f4 v[108:111], v[24:31], v[52:59], v[108:111], v198, v198 op_sel_hi:[0,0,0]
	s_waitcnt lgkmcnt(0)
	v_mfma_scale_f32_16x16x128_f8f6f4 v[104:107], v[16:23], v[218:225], v[104:107], v198, v198 op_sel_hi:[0,0,0]
	v_mfma_scale_f32_16x16x128_f8f6f4 v[100:103], v[24:31], v[218:225], v[100:103], v198, v198 op_sel_hi:[0,0,0]
	s_setprio 0
	s_setprio 1
	v_mfma_scale_f32_16x16x128_f8f6f4 v[96:99], v[8:15], v[36:43], v[96:99], v198, v198 op_sel_hi:[0,0,0]
	v_mfma_scale_f32_16x16x128_f8f6f4 v[92:95], v[0:7], v[36:43], v[92:95], v198, v198 op_sel_hi:[0,0,0]
	v_mfma_scale_f32_16x16x128_f8f6f4 v[88:91], v[8:15], v[44:51], v[88:91], v198, v198 op_sel_hi:[0,0,0]
	v_mfma_scale_f32_16x16x128_f8f6f4 v[84:87], v[0:7], v[44:51], v[84:87], v198, v198 op_sel_hi:[0,0,0]
	v_mfma_scale_f32_16x16x128_f8f6f4 v[80:83], v[8:15], v[52:59], v[80:83], v198, v198 op_sel_hi:[0,0,0]
	v_mfma_scale_f32_16x16x128_f8f6f4 v[76:79], v[0:7], v[52:59], v[76:79], v198, v198 op_sel_hi:[0,0,0]
	v_mfma_scale_f32_16x16x128_f8f6f4 v[72:75], v[8:15], v[218:225], v[72:75], v198, v198 op_sel_hi:[0,0,0]
	v_mfma_scale_f32_16x16x128_f8f6f4 v[68:71], v[0:7], v[218:225], v[68:71], v198, v198 op_sel_hi:[0,0,0]
	s_setprio 0
	s_barrier
	ds_read_b128 v[24:27], v202 offset:0x8000
	ds_read_b128 v[28:31], v202 offset:0x8400
	ds_read_b128 v[16:19], v202 offset:0x8800
	ds_read_b128 v[20:23], v202 offset:0x8c00
	ds_read_b128 v[36:39], v201 offset:0x8000
	ds_read_b128 v[40:43], v201 offset:0x8400
	ds_read_b128 v[44:47], v201 offset:0x8800
	ds_read_b128 v[48:51], v201 offset:0x8c00
	ds_read_b128 v[52:55], v201 offset:0x9000
	ds_read_b128 v[56:59], v201 offset:0x9400
	ds_read_b128 v[218:221], v201 offset:0x9800
	ds_read_b128 v[222:225], v201 offset:0x9c00
	ds_read_b128 v[8:11], v202 offset:0xc000
	ds_read_b128 v[12:15], v202 offset:0xc400
	ds_read_b128 v[0:3], v202 offset:0xc800
	ds_read_b128 v[4:7], v202 offset:0xcc00
	s_mov_b32 m0, s50
	v_cndmask_b32_e32 v62, v207, v34, vcc
	buffer_load_dwordx4 v62, s[4:7], s67 offen lds
	v_cndmask_b32_e32 v62, v206, v35, vcc
	s_mov_b32 m0, s51
	s_nop 0
	buffer_load_dwordx4 v62, s[4:7], s67 offen lds
	s_waitcnt vmcnt(8)
	s_waitcnt lgkmcnt(8)
	s_barrier
	s_setprio 1
	v_mfma_scale_f32_16x16x128_f8f6f4 v[192:195], v[24:31], v[36:43], v[192:195], v198, v198 op_sel_hi:[0,0,0]
	v_mfma_scale_f32_16x16x128_f8f6f4 v[188:191], v[16:23], v[36:43], v[188:191], v198, v198 op_sel_hi:[0,0,0]
	v_mfma_scale_f32_16x16x128_f8f6f4 v[184:187], v[24:31], v[44:51], v[184:187], v198, v198 op_sel_hi:[0,0,0]
	v_mfma_scale_f32_16x16x128_f8f6f4 v[180:183], v[16:23], v[44:51], v[180:183], v198, v198 op_sel_hi:[0,0,0]
	s_waitcnt lgkmcnt(6)
	v_mfma_scale_f32_16x16x128_f8f6f4 v[176:179], v[24:31], v[52:59], v[176:179], v198, v198 op_sel_hi:[0,0,0]
	v_mfma_scale_f32_16x16x128_f8f6f4 v[172:175], v[16:23], v[52:59], v[172:175], v198, v198 op_sel_hi:[0,0,0]
	s_waitcnt lgkmcnt(4)
	v_mfma_scale_f32_16x16x128_f8f6f4 v[168:171], v[24:31], v[218:225], v[168:171], v198, v198 op_sel_hi:[0,0,0]
	v_mfma_scale_f32_16x16x128_f8f6f4 v[164:167], v[16:23], v[218:225], v[164:167], v198, v198 op_sel_hi:[0,0,0]
	s_setprio 0
	s_setprio 1
	s_waitcnt lgkmcnt(2)
	v_mfma_scale_f32_16x16x128_f8f6f4 v[160:163], v[8:15], v[36:43], v[160:163], v198, v198 op_sel_hi:[0,0,0]
	s_waitcnt lgkmcnt(0)
	v_mfma_scale_f32_16x16x128_f8f6f4 v[156:159], v[0:7], v[36:43], v[156:159], v198, v198 op_sel_hi:[0,0,0]
	v_mfma_scale_f32_16x16x128_f8f6f4 v[152:155], v[8:15], v[44:51], v[152:155], v198, v198 op_sel_hi:[0,0,0]
	v_mfma_scale_f32_16x16x128_f8f6f4 v[148:151], v[0:7], v[44:51], v[148:151], v198, v198 op_sel_hi:[0,0,0]
	v_mfma_scale_f32_16x16x128_f8f6f4 v[144:147], v[8:15], v[52:59], v[144:147], v198, v198 op_sel_hi:[0,0,0]
	v_mfma_scale_f32_16x16x128_f8f6f4 v[140:143], v[0:7], v[52:59], v[140:143], v198, v198 op_sel_hi:[0,0,0]
	v_mfma_scale_f32_16x16x128_f8f6f4 v[136:139], v[8:15], v[218:225], v[136:139], v198, v198 op_sel_hi:[0,0,0]
	v_mfma_scale_f32_16x16x128_f8f6f4 v[132:135], v[0:7], v[218:225], v[132:135], v198, v198 op_sel_hi:[0,0,0]
	s_setprio 0
	s_barrier
	ds_read_b128 v[36:39], v201 offset:0xc000
	ds_read_b128 v[40:43], v201 offset:0xc400
	ds_read_b128 v[44:47], v201 offset:0xc800
	ds_read_b128 v[48:51], v201 offset:0xcc00
	ds_read_b128 v[52:55], v201 offset:0xd000
	ds_read_b128 v[56:59], v201 offset:0xd400
	ds_read_b128 v[218:221], v201 offset:0xd800
	ds_read_b128 v[222:225], v201 offset:0xdc00
	s_mov_b32 m0, s64
	s_add_i32 s67, s66, 0x80
	buffer_load_dwordx4 v200, s[8:11], s67 offen lds
	s_add_i32 s67, s66, 0x80080
	s_mov_b32 m0, s65
	s_nop 0
	buffer_load_dwordx4 v200, s[8:11], s67 offen lds
	s_add_i32 s67, s66, 0x8080
	s_mov_b32 m0, s70
	s_add_i32 s66, s66, 0x88080
	buffer_load_dwordx4 v200, s[8:11], s67 offen lds
	s_mov_b32 m0, s71
	s_nop 0
	buffer_load_dwordx4 v200, s[8:11], s66 offen lds
	s_mov_b32 m0, s68
	s_nop 0
	buffer_load_dwordx4 v60, s[4:7], s61 offen lds
	s_mov_b32 m0, s69
	s_nop 0
	buffer_load_dwordx4 v61, s[4:7], s61 offen lds
	s_waitcnt vmcnt(8)
	s_waitcnt lgkmcnt(6)
	s_barrier
	s_setprio 1
	v_mfma_scale_f32_16x16x128_f8f6f4 v[128:131], v[24:31], v[36:43], v[128:131], v198, v198 op_sel_hi:[0,0,0]
	v_mfma_scale_f32_16x16x128_f8f6f4 v[124:127], v[16:23], v[36:43], v[124:127], v198, v198 op_sel_hi:[0,0,0]
	s_waitcnt lgkmcnt(4)
	v_mfma_scale_f32_16x16x128_f8f6f4 v[120:123], v[24:31], v[44:51], v[120:123], v198, v198 op_sel_hi:[0,0,0]
	v_mfma_scale_f32_16x16x128_f8f6f4 v[116:119], v[16:23], v[44:51], v[116:119], v198, v198 op_sel_hi:[0,0,0]
	s_waitcnt lgkmcnt(2)
	v_mfma_scale_f32_16x16x128_f8f6f4 v[112:115], v[24:31], v[52:59], v[112:115], v198, v198 op_sel_hi:[0,0,0]
	v_mfma_scale_f32_16x16x128_f8f6f4 v[108:111], v[16:23], v[52:59], v[108:111], v198, v198 op_sel_hi:[0,0,0]
	s_waitcnt lgkmcnt(0)
	v_mfma_scale_f32_16x16x128_f8f6f4 v[104:107], v[24:31], v[218:225], v[104:107], v198, v198 op_sel_hi:[0,0,0]
	v_mfma_scale_f32_16x16x128_f8f6f4 v[100:103], v[16:23], v[218:225], v[100:103], v198, v198 op_sel_hi:[0,0,0]
	s_setprio 0
	s_setprio 1
	v_mfma_scale_f32_16x16x128_f8f6f4 v[96:99], v[8:15], v[36:43], v[96:99], v198, v198 op_sel_hi:[0,0,0]
	v_mfma_scale_f32_16x16x128_f8f6f4 v[92:95], v[0:7], v[36:43], v[92:95], v198, v198 op_sel_hi:[0,0,0]
	v_mfma_scale_f32_16x16x128_f8f6f4 v[88:91], v[8:15], v[44:51], v[88:91], v198, v198 op_sel_hi:[0,0,0]
	v_mfma_scale_f32_16x16x128_f8f6f4 v[84:87], v[0:7], v[44:51], v[84:87], v198, v198 op_sel_hi:[0,0,0]
	v_mfma_scale_f32_16x16x128_f8f6f4 v[80:83], v[8:15], v[52:59], v[80:83], v198, v198 op_sel_hi:[0,0,0]
	v_mfma_scale_f32_16x16x128_f8f6f4 v[76:79], v[0:7], v[52:59], v[76:79], v198, v198 op_sel_hi:[0,0,0]
	v_mfma_scale_f32_16x16x128_f8f6f4 v[72:75], v[8:15], v[218:225], v[72:75], v198, v198 op_sel_hi:[0,0,0]
	v_mfma_scale_f32_16x16x128_f8f6f4 v[68:71], v[0:7], v[218:225], v[68:71], v198, v198 op_sel_hi:[0,0,0]
	s_setprio 0
	s_barrier
	s_add_i32 s37, s37, 2
	s_addk_i32 s36, 0x100
	s_addk_i32 s33, 0x100
	s_cmp_gt_u32 s37, 29
	s_cbranch_scc0 .LBB0_1330
	s_and_b64 vcc, exec, s[28:29]
	s_cbranch_vccz .LBB0_1333
	s_barrier

.LBB0_1369:
	s_add_i32 s33, s88, 0x180
	s_add_i32 s40, s89, 0x180
	s_waitcnt lgkmcnt(6)
	s_barrier
	s_setprio 1
	v_mfma_scale_f32_16x16x128_f8f6f4 v[128:131], v[24:31], v[56:63], 0, v235, v235 op_sel_hi:[0,0,0]
	v_mfma_scale_f32_16x16x128_f8f6f4 v[124:127], v[16:23], v[56:63], 0, v235, v235 op_sel_hi:[0,0,0]
	s_waitcnt lgkmcnt(4)
	v_mfma_scale_f32_16x16x128_f8f6f4 v[120:123], v[24:31], v[48:55], 0, v235, v235 op_sel_hi:[0,0,0]
	v_mfma_scale_f32_16x16x128_f8f6f4 v[116:119], v[16:23], v[48:55], 0, v235, v235 op_sel_hi:[0,0,0]
	s_waitcnt lgkmcnt(2)
	v_mfma_scale_f32_16x16x128_f8f6f4 v[112:115], v[24:31], v[40:47], 0, v235, v235 op_sel_hi:[0,0,0]
	v_mfma_scale_f32_16x16x128_f8f6f4 v[108:111], v[16:23], v[40:47], 0, v235, v235 op_sel_hi:[0,0,0]
	s_waitcnt lgkmcnt(0)
	v_mfma_scale_f32_16x16x128_f8f6f4 v[104:107], v[24:31], v[32:39], 0, v235, v235 op_sel_hi:[0,0,0]
	v_mfma_scale_f32_16x16x128_f8f6f4 v[100:103], v[16:23], v[32:39], 0, v235, v235 op_sel_hi:[0,0,0]
	s_setprio 0
	s_setprio 1
	v_mfma_scale_f32_16x16x128_f8f6f4 v[96:99], v[8:15], v[56:63], 0, v235, v235 op_sel_hi:[0,0,0]
	v_mfma_scale_f32_16x16x128_f8f6f4 v[92:95], v[0:7], v[56:63], 0, v235, v235 op_sel_hi:[0,0,0]
	v_mfma_scale_f32_16x16x128_f8f6f4 v[88:91], v[8:15], v[48:55], 0, v235, v235 op_sel_hi:[0,0,0]
	v_mfma_scale_f32_16x16x128_f8f6f4 v[84:87], v[0:7], v[48:55], 0, v235, v235 op_sel_hi:[0,0,0]
	v_mfma_scale_f32_16x16x128_f8f6f4 v[80:83], v[8:15], v[40:47], 0, v235, v235 op_sel_hi:[0,0,0]
	v_mfma_scale_f32_16x16x128_f8f6f4 v[76:79], v[0:7], v[40:47], 0, v235, v235 op_sel_hi:[0,0,0]
	v_mfma_scale_f32_16x16x128_f8f6f4 v[72:75], v[8:15], v[32:39], 0, v235, v235 op_sel_hi:[0,0,0]
	v_mfma_scale_f32_16x16x128_f8f6f4 v[68:71], v[0:7], v[32:39], 0, v235, v235 op_sel_hi:[0,0,0]
	s_setprio 0
	s_barrier
	ds_read_b128 v[16:19], v233 offset:0x8000
	ds_read_b128 v[20:23], v233 offset:0x8400
	ds_read_b128 v[24:27], v233 offset:0x8800
	ds_read_b128 v[28:31], v233 offset:0x8c00
	ds_read_b128 v[32:35], v232 offset:0x8000
	ds_read_b128 v[36:39], v232 offset:0x8400
	ds_read_b128 v[40:43], v232 offset:0x8800
	ds_read_b128 v[44:47], v232 offset:0x8c00
	ds_read_b128 v[48:51], v232 offset:0x9000
	ds_read_b128 v[52:55], v232 offset:0x9400
	ds_read_b128 v[56:59], v232 offset:0x9800
	ds_read_b128 v[60:63], v232 offset:0x9c00
	ds_read_b128 v[8:11], v233 offset:0xc000
	ds_read_b128 v[12:15], v233 offset:0xc400
	ds_read_b128 v[0:3], v233 offset:0xc800
	ds_read_b128 v[4:7], v233 offset:0xcc00
	s_mov_b32 m0, s62
	s_add_i32 s10, s88, 0x10100
	buffer_load_dwordx4 v230, s[4:7], s10 offen lds
	s_add_i32 s10, s88, 0x18100
	s_mov_b32 m0, s63
	s_nop 0
	buffer_load_dwordx4 v230, s[4:7], s10 offen lds
	s_waitcnt vmcnt(8)
	s_waitcnt lgkmcnt(8)
	s_barrier
	s_setprio 1
	v_mfma_scale_f32_16x16x128_f8f6f4 v[192:195], v[16:23], v[32:39], v[192:195], v235, v235 op_sel_hi:[0,0,0]
	v_mfma_scale_f32_16x16x128_f8f6f4 v[188:191], v[24:31], v[32:39], v[188:191], v235, v235 op_sel_hi:[0,0,0]
	v_mfma_scale_f32_16x16x128_f8f6f4 v[184:187], v[16:23], v[40:47], v[184:187], v235, v235 op_sel_hi:[0,0,0]
	v_mfma_scale_f32_16x16x128_f8f6f4 v[180:183], v[24:31], v[40:47], v[180:183], v235, v235 op_sel_hi:[0,0,0]
	s_waitcnt lgkmcnt(6)
	v_mfma_scale_f32_16x16x128_f8f6f4 v[176:179], v[16:23], v[48:55], v[176:179], v235, v235 op_sel_hi:[0,0,0]
	v_mfma_scale_f32_16x16x128_f8f6f4 v[172:175], v[24:31], v[48:55], v[172:175], v235, v235 op_sel_hi:[0,0,0]
	s_waitcnt lgkmcnt(4)
	v_mfma_scale_f32_16x16x128_f8f6f4 v[168:171], v[16:23], v[56:63], v[168:171], v235, v235 op_sel_hi:[0,0,0]
	v_mfma_scale_f32_16x16x128_f8f6f4 v[164:167], v[24:31], v[56:63], v[164:167], v235, v235 op_sel_hi:[0,0,0]
	s_setprio 0
	s_setprio 1
	s_waitcnt lgkmcnt(2)
	v_mfma_scale_f32_16x16x128_f8f6f4 v[160:163], v[8:15], v[32:39], v[160:163], v235, v235 op_sel_hi:[0,0,0]
	s_waitcnt lgkmcnt(0)
	v_mfma_scale_f32_16x16x128_f8f6f4 v[156:159], v[0:7], v[32:39], v[156:159], v235, v235 op_sel_hi:[0,0,0]
	v_mfma_scale_f32_16x16x128_f8f6f4 v[152:155], v[8:15], v[40:47], v[152:155], v235, v235 op_sel_hi:[0,0,0]
	v_mfma_scale_f32_16x16x128_f8f6f4 v[148:151], v[0:7], v[40:47], v[148:151], v235, v235 op_sel_hi:[0,0,0]
	v_mfma_scale_f32_16x16x128_f8f6f4 v[144:147], v[8:15], v[48:55], v[144:147], v235, v235 op_sel_hi:[0,0,0]
	v_mfma_scale_f32_16x16x128_f8f6f4 v[140:143], v[0:7], v[48:55], v[140:143], v235, v235 op_sel_hi:[0,0,0]
	v_mfma_scale_f32_16x16x128_f8f6f4 v[136:139], v[8:15], v[56:63], v[136:139], v235, v235 op_sel_hi:[0,0,0]
	v_mfma_scale_f32_16x16x128_f8f6f4 v[132:135], v[0:7], v[56:63], v[132:135], v235, v235 op_sel_hi:[0,0,0]
	s_setprio 0
	s_barrier
	ds_read_b128 v[32:35], v232 offset:0xc000
	ds_read_b128 v[36:39], v232 offset:0xc400
	ds_read_b128 v[40:43], v232 offset:0xc800
	ds_read_b128 v[44:47], v232 offset:0xcc00
	ds_read_b128 v[48:51], v232 offset:0xd000
	ds_read_b128 v[52:55], v232 offset:0xd400
	ds_read_b128 v[56:59], v232 offset:0xd800
	ds_read_b128 v[60:63], v232 offset:0xdc00
	s_mov_b32 m0, s64
	s_mov_b32 s10, s6
	s_mov_b32 s11, s7
	buffer_load_dwordx4 v231, s[8:11], s40 offen lds
	s_add_i32 s40, s89, 0x10180
	s_mov_b32 m0, s65
	s_nop 0
	buffer_load_dwordx4 v231, s[8:11], s40 offen lds
	s_add_i32 s40, s89, 0x1180
	s_mov_b32 m0, s70
	s_nop 0
	buffer_load_dwordx4 v231, s[8:11], s40 offen lds
	s_add_i32 s40, s89, 0x11180
	s_mov_b32 m0, s71
	s_nop 0
	buffer_load_dwordx4 v231, s[8:11], s40 offen lds
	s_mov_b32 m0, s68
	s_nop 0
	buffer_load_dwordx4 v230, s[4:7], s33 offen lds
	s_add_i32 s33, s88, 0x8180
	s_mov_b32 m0, s69
	s_nop 0
	buffer_load_dwordx4 v230, s[4:7], s33 offen lds
	s_waitcnt vmcnt(8)
	s_waitcnt lgkmcnt(6)
	s_barrier
	s_setprio 1
	v_mfma_scale_f32_16x16x128_f8f6f4 v[128:131], v[16:23], v[32:39], v[128:131], v235, v235 op_sel_hi:[0,0,0]
	v_mfma_scale_f32_16x16x128_f8f6f4 v[124:127], v[24:31], v[32:39], v[124:127], v235, v235 op_sel_hi:[0,0,0]
	s_waitcnt lgkmcnt(4)
	v_mfma_scale_f32_16x16x128_f8f6f4 v[120:123], v[16:23], v[40:47], v[120:123], v235, v235 op_sel_hi:[0,0,0]
	v_mfma_scale_f32_16x16x128_f8f6f4 v[116:119], v[24:31], v[40:47], v[116:119], v235, v235 op_sel_hi:[0,0,0]
	s_waitcnt lgkmcnt(2)
	v_mfma_scale_f32_16x16x128_f8f6f4 v[112:115], v[16:23], v[48:55], v[112:115], v235, v235 op_sel_hi:[0,0,0]
	v_mfma_scale_f32_16x16x128_f8f6f4 v[108:111], v[24:31], v[48:55], v[108:111], v235, v235 op_sel_hi:[0,0,0]
	s_waitcnt lgkmcnt(0)
	v_mfma_scale_f32_16x16x128_f8f6f4 v[104:107], v[16:23], v[56:63], v[104:107], v235, v235 op_sel_hi:[0,0,0]
	v_mfma_scale_f32_16x16x128_f8f6f4 v[100:103], v[24:31], v[56:63], v[100:103], v235, v235 op_sel_hi:[0,0,0]
	s_setprio 0
	s_setprio 1
	v_mfma_scale_f32_16x16x128_f8f6f4 v[96:99], v[8:15], v[32:39], v[96:99], v235, v235 op_sel_hi:[0,0,0]
	v_mfma_scale_f32_16x16x128_f8f6f4 v[92:95], v[0:7], v[32:39], v[92:95], v235, v235 op_sel_hi:[0,0,0]
	v_mfma_scale_f32_16x16x128_f8f6f4 v[88:91], v[8:15], v[40:47], v[88:91], v235, v235 op_sel_hi:[0,0,0]
	v_mfma_scale_f32_16x16x128_f8f6f4 v[84:87], v[0:7], v[40:47], v[84:87], v235, v235 op_sel_hi:[0,0,0]
	v_mfma_scale_f32_16x16x128_f8f6f4 v[80:83], v[8:15], v[48:55], v[80:83], v235, v235 op_sel_hi:[0,0,0]
	v_mfma_scale_f32_16x16x128_f8f6f4 v[76:79], v[0:7], v[48:55], v[76:79], v235, v235 op_sel_hi:[0,0,0]
	v_mfma_scale_f32_16x16x128_f8f6f4 v[72:75], v[8:15], v[56:63], v[72:75], v235, v235 op_sel_hi:[0,0,0]
	v_mfma_scale_f32_16x16x128_f8f6f4 v[68:71], v[0:7], v[56:63], v[68:71], v235, v235 op_sel_hi:[0,0,0]
	s_setprio 0
	s_barrier
	ds_read_b128 v[16:19], v233 offset:0
	ds_read_b128 v[20:23], v233 offset:0x400
	ds_read_b128 v[24:27], v233 offset:0x800
	ds_read_b128 v[28:31], v233 offset:0xc00
	ds_read_b128 v[32:35], v232 offset:0
	ds_read_b128 v[36:39], v232 offset:0x400
	ds_read_b128 v[40:43], v232 offset:0x800
	ds_read_b128 v[44:47], v232 offset:0xc00
	ds_read_b128 v[48:51], v232 offset:0x1000
	ds_read_b128 v[52:55], v232 offset:0x1400
	ds_read_b128 v[56:59], v232 offset:0x1800
	ds_read_b128 v[60:63], v232 offset:0x1c00
	ds_read_b128 v[8:11], v233 offset:0x4000
	ds_read_b128 v[12:15], v233 offset:0x4400
	ds_read_b128 v[0:3], v233 offset:0x4800
	ds_read_b128 v[4:7], v233 offset:0x4c00
	s_add_i32 s33, s85, 0x80
	s_mov_b32 m0, s74
	s_add_i32 s40, s88, 0x10180
	buffer_load_dwordx4 v230, s[4:7], s40 offen lds
	s_add_i32 s40, s88, 0x18180
	s_mov_b32 m0, s76
	s_nop 0
	buffer_load_dwordx4 v230, s[4:7], s40 offen lds
	s_waitcnt vmcnt(8)
	s_waitcnt lgkmcnt(8)
	s_barrier
	s_setprio 1
	v_mfma_scale_f32_16x16x128_f8f6f4 v[192:195], v[16:23], v[32:39], v[192:195], v235, v235 op_sel_hi:[0,0,0]
	v_mfma_scale_f32_16x16x128_f8f6f4 v[188:191], v[24:31], v[32:39], v[188:191], v235, v235 op_sel_hi:[0,0,0]
	v_mfma_scale_f32_16x16x128_f8f6f4 v[184:187], v[16:23], v[40:47], v[184:187], v235, v235 op_sel_hi:[0,0,0]
	v_mfma_scale_f32_16x16x128_f8f6f4 v[180:183], v[24:31], v[40:47], v[180:183], v235, v235 op_sel_hi:[0,0,0]
	s_waitcnt lgkmcnt(6)
	v_mfma_scale_f32_16x16x128_f8f6f4 v[176:179], v[16:23], v[48:55], v[176:179], v235, v235 op_sel_hi:[0,0,0]
	v_mfma_scale_f32_16x16x128_f8f6f4 v[172:175], v[24:31], v[48:55], v[172:175], v235, v235 op_sel_hi:[0,0,0]
	s_waitcnt lgkmcnt(4)
	v_mfma_scale_f32_16x16x128_f8f6f4 v[168:171], v[16:23], v[56:63], v[168:171], v235, v235 op_sel_hi:[0,0,0]
	v_mfma_scale_f32_16x16x128_f8f6f4 v[164:167], v[24:31], v[56:63], v[164:167], v235, v235 op_sel_hi:[0,0,0]
	s_setprio 0
	s_setprio 1
	s_waitcnt lgkmcnt(2)
	v_mfma_scale_f32_16x16x128_f8f6f4 v[160:163], v[8:15], v[32:39], v[160:163], v235, v235 op_sel_hi:[0,0,0]
	s_waitcnt lgkmcnt(0)
	v_mfma_scale_f32_16x16x128_f8f6f4 v[156:159], v[0:7], v[32:39], v[156:159], v235, v235 op_sel_hi:[0,0,0]
	v_mfma_scale_f32_16x16x128_f8f6f4 v[152:155], v[8:15], v[40:47], v[152:155], v235, v235 op_sel_hi:[0,0,0]
	v_mfma_scale_f32_16x16x128_f8f6f4 v[148:151], v[0:7], v[40:47], v[148:151], v235, v235 op_sel_hi:[0,0,0]
	v_mfma_scale_f32_16x16x128_f8f6f4 v[144:147], v[8:15], v[48:55], v[144:147], v235, v235 op_sel_hi:[0,0,0]
	v_mfma_scale_f32_16x16x128_f8f6f4 v[140:143], v[0:7], v[48:55], v[140:143], v235, v235 op_sel_hi:[0,0,0]
	v_mfma_scale_f32_16x16x128_f8f6f4 v[136:139], v[8:15], v[56:63], v[136:139], v235, v235 op_sel_hi:[0,0,0]
	v_mfma_scale_f32_16x16x128_f8f6f4 v[132:135], v[0:7], v[56:63], v[132:135], v235, v235 op_sel_hi:[0,0,0]
	s_setprio 0
	s_barrier
	ds_read_b128 v[32:35], v232 offset:0x4000
	ds_read_b128 v[36:39], v232 offset:0x4400
	ds_read_b128 v[40:43], v232 offset:0x4800
	ds_read_b128 v[44:47], v232 offset:0x4c00
	ds_read_b128 v[48:51], v232 offset:0x5000
	ds_read_b128 v[52:55], v232 offset:0x5400
	ds_read_b128 v[56:59], v232 offset:0x5800
	ds_read_b128 v[60:63], v232 offset:0x5c00
	s_mov_b32 m0, s46
	s_nop 0
	buffer_load_dwordx4 v231, s[8:11], s86 offen lds
	s_add_i32 s40, s86, 0x10000
	s_mov_b32 m0, s47
	s_nop 0
	buffer_load_dwordx4 v231, s[8:11], s40 offen lds
	s_add_i32 s40, s86, 0x1000
	s_mov_b32 m0, s49
	s_nop 0
	buffer_load_dwordx4 v231, s[8:11], s40 offen lds
	s_add_i32 s40, s86, 0x11000
	s_mov_b32 m0, s50
	s_nop 0
	buffer_load_dwordx4 v231, s[8:11], s40 offen lds
	s_mov_b32 m0, s48
	s_add_i32 s40, s85, 0x8000
	buffer_load_dwordx4 v230, s[4:7], s85 offen lds
	s_mov_b32 m0, s51
	s_nop 0
	buffer_load_dwordx4 v230, s[4:7], s40 offen lds
	s_waitcnt vmcnt(8)
	s_waitcnt lgkmcnt(6)
	s_barrier
	s_setprio 1
	v_mfma_scale_f32_16x16x128_f8f6f4 v[128:131], v[16:23], v[32:39], v[128:131], v235, v235 op_sel_hi:[0,0,0]
	v_mfma_scale_f32_16x16x128_f8f6f4 v[124:127], v[24:31], v[32:39], v[124:127], v235, v235 op_sel_hi:[0,0,0]
	s_waitcnt lgkmcnt(4)
	v_mfma_scale_f32_16x16x128_f8f6f4 v[120:123], v[16:23], v[40:47], v[120:123], v235, v235 op_sel_hi:[0,0,0]
	v_mfma_scale_f32_16x16x128_f8f6f4 v[116:119], v[24:31], v[40:47], v[116:119], v235, v235 op_sel_hi:[0,0,0]
	s_waitcnt lgkmcnt(2)
	v_mfma_scale_f32_16x16x128_f8f6f4 v[112:115], v[16:23], v[48:55], v[112:115], v235, v235 op_sel_hi:[0,0,0]
	v_mfma_scale_f32_16x16x128_f8f6f4 v[108:111], v[24:31], v[48:55], v[108:111], v235, v235 op_sel_hi:[0,0,0]
	s_waitcnt lgkmcnt(0)
	v_mfma_scale_f32_16x16x128_f8f6f4 v[104:107], v[16:23], v[56:63], v[104:107], v235, v235 op_sel_hi:[0,0,0]
	v_mfma_scale_f32_16x16x128_f8f6f4 v[100:103], v[24:31], v[56:63], v[100:103], v235, v235 op_sel_hi:[0,0,0]
	s_setprio 0
	s_setprio 1
	v_mfma_scale_f32_16x16x128_f8f6f4 v[96:99], v[8:15], v[32:39], v[96:99], v235, v235 op_sel_hi:[0,0,0]
	v_mfma_scale_f32_16x16x128_f8f6f4 v[92:95], v[0:7], v[32:39], v[92:95], v235, v235 op_sel_hi:[0,0,0]
	v_mfma_scale_f32_16x16x128_f8f6f4 v[88:91], v[8:15], v[40:47], v[88:91], v235, v235 op_sel_hi:[0,0,0]
	v_mfma_scale_f32_16x16x128_f8f6f4 v[84:87], v[0:7], v[40:47], v[84:87], v235, v235 op_sel_hi:[0,0,0]
	v_mfma_scale_f32_16x16x128_f8f6f4 v[80:83], v[8:15], v[48:55], v[80:83], v235, v235 op_sel_hi:[0,0,0]
	v_mfma_scale_f32_16x16x128_f8f6f4 v[76:79], v[0:7], v[48:55], v[76:79], v235, v235 op_sel_hi:[0,0,0]
	v_mfma_scale_f32_16x16x128_f8f6f4 v[72:75], v[8:15], v[56:63], v[72:75], v235, v235 op_sel_hi:[0,0,0]
	v_mfma_scale_f32_16x16x128_f8f6f4 v[68:71], v[0:7], v[56:63], v[68:71], v235, v235 op_sel_hi:[0,0,0]
	s_setprio 0
	s_barrier
	ds_read_b128 v[16:19], v233 offset:0x8000
	ds_read_b128 v[20:23], v233 offset:0x8400
	ds_read_b128 v[24:27], v233 offset:0x8800
	ds_read_b128 v[28:31], v233 offset:0x8c00
	ds_read_b128 v[32:35], v232 offset:0x8000
	ds_read_b128 v[36:39], v232 offset:0x8400
	ds_read_b128 v[40:43], v232 offset:0x8800
	ds_read_b128 v[44:47], v232 offset:0x8c00
	ds_read_b128 v[48:51], v232 offset:0x9000
	ds_read_b128 v[52:55], v232 offset:0x9400
	ds_read_b128 v[56:59], v232 offset:0x9800
	ds_read_b128 v[60:63], v232 offset:0x9c00
	ds_read_b128 v[8:11], v233 offset:0xc000
	ds_read_b128 v[12:15], v233 offset:0xc400
	ds_read_b128 v[0:3], v233 offset:0xc800
	ds_read_b128 v[4:7], v233 offset:0xcc00
	s_mov_b32 m0, s62
	s_add_i32 s40, s85, 0x10000
	buffer_load_dwordx4 v230, s[4:7], s40 offen lds
	s_add_i32 s40, s85, 0x18000
	s_mov_b32 m0, s63
	s_nop 0
	buffer_load_dwordx4 v230, s[4:7], s40 offen lds
	s_waitcnt vmcnt(8)
	s_waitcnt lgkmcnt(8)
	s_barrier
	s_setprio 1
	v_mfma_scale_f32_16x16x128_f8f6f4 v[192:195], v[16:23], v[32:39], v[192:195], v235, v235 op_sel_hi:[0,0,0]
	v_mfma_scale_f32_16x16x128_f8f6f4 v[188:191], v[24:31], v[32:39], v[188:191], v235, v235 op_sel_hi:[0,0,0]
	v_mfma_scale_f32_16x16x128_f8f6f4 v[184:187], v[16:23], v[40:47], v[184:187], v235, v235 op_sel_hi:[0,0,0]
	v_mfma_scale_f32_16x16x128_f8f6f4 v[180:183], v[24:31], v[40:47], v[180:183], v235, v235 op_sel_hi:[0,0,0]
	s_waitcnt lgkmcnt(6)
	v_mfma_scale_f32_16x16x128_f8f6f4 v[176:179], v[16:23], v[48:55], v[176:179], v235, v235 op_sel_hi:[0,0,0]
	v_mfma_scale_f32_16x16x128_f8f6f4 v[172:175], v[24:31], v[48:55], v[172:175], v235, v235 op_sel_hi:[0,0,0]
	s_waitcnt lgkmcnt(4)
	v_mfma_scale_f32_16x16x128_f8f6f4 v[168:171], v[16:23], v[56:63], v[168:171], v235, v235 op_sel_hi:[0,0,0]
	v_mfma_scale_f32_16x16x128_f8f6f4 v[164:167], v[24:31], v[56:63], v[164:167], v235, v235 op_sel_hi:[0,0,0]
	s_setprio 0
	s_setprio 1
	s_waitcnt lgkmcnt(2)
	v_mfma_scale_f32_16x16x128_f8f6f4 v[160:163], v[8:15], v[32:39], v[160:163], v235, v235 op_sel_hi:[0,0,0]
	s_waitcnt lgkmcnt(0)
	v_mfma_scale_f32_16x16x128_f8f6f4 v[156:159], v[0:7], v[32:39], v[156:159], v235, v235 op_sel_hi:[0,0,0]
	v_mfma_scale_f32_16x16x128_f8f6f4 v[152:155], v[8:15], v[40:47], v[152:155], v235, v235 op_sel_hi:[0,0,0]
	v_mfma_scale_f32_16x16x128_f8f6f4 v[148:151], v[0:7], v[40:47], v[148:151], v235, v235 op_sel_hi:[0,0,0]
	v_mfma_scale_f32_16x16x128_f8f6f4 v[144:147], v[8:15], v[48:55], v[144:147], v235, v235 op_sel_hi:[0,0,0]
	v_mfma_scale_f32_16x16x128_f8f6f4 v[140:143], v[0:7], v[48:55], v[140:143], v235, v235 op_sel_hi:[0,0,0]
	v_mfma_scale_f32_16x16x128_f8f6f4 v[136:139], v[8:15], v[56:63], v[136:139], v235, v235 op_sel_hi:[0,0,0]
	v_mfma_scale_f32_16x16x128_f8f6f4 v[132:135], v[0:7], v[56:63], v[132:135], v235, v235 op_sel_hi:[0,0,0]
	s_setprio 0
	s_barrier
	ds_read_b128 v[32:35], v232 offset:0xc000
	ds_read_b128 v[36:39], v232 offset:0xc400
	ds_read_b128 v[40:43], v232 offset:0xc800
	ds_read_b128 v[44:47], v232 offset:0xcc00
	ds_read_b128 v[48:51], v232 offset:0xd000
	ds_read_b128 v[52:55], v232 offset:0xd400
	ds_read_b128 v[56:59], v232 offset:0xd800
	ds_read_b128 v[60:63], v232 offset:0xdc00
	s_mov_b32 m0, s64
	s_add_i32 s40, s86, 0x80
	buffer_load_dwordx4 v231, s[8:11], s40 offen lds
	s_add_i32 s40, s86, 0x10080
	s_mov_b32 m0, s65
	s_nop 0
	buffer_load_dwordx4 v231, s[8:11], s40 offen lds
	s_add_i32 s40, s86, 0x1080
	s_mov_b32 m0, s70
	s_nop 0
	buffer_load_dwordx4 v231, s[8:11], s40 offen lds
	s_add_i32 s40, s86, 0x11080
	s_mov_b32 m0, s71
	s_nop 0
	buffer_load_dwordx4 v231, s[8:11], s40 offen lds
	s_mov_b32 m0, s68
	s_add_i32 s10, s85, 0x8080
	buffer_load_dwordx4 v230, s[4:7], s33 offen lds
	s_mov_b32 m0, s69
	s_nop 0
	buffer_load_dwordx4 v230, s[4:7], s10 offen lds
	s_waitcnt vmcnt(8)
	s_waitcnt lgkmcnt(6)
	s_barrier
	s_setprio 1
	v_mfma_scale_f32_16x16x128_f8f6f4 v[128:131], v[16:23], v[32:39], v[128:131], v235, v235 op_sel_hi:[0,0,0]
	v_mfma_scale_f32_16x16x128_f8f6f4 v[124:127], v[24:31], v[32:39], v[124:127], v235, v235 op_sel_hi:[0,0,0]
	s_waitcnt lgkmcnt(4)
	v_mfma_scale_f32_16x16x128_f8f6f4 v[120:123], v[16:23], v[40:47], v[120:123], v235, v235 op_sel_hi:[0,0,0]
	v_mfma_scale_f32_16x16x128_f8f6f4 v[116:119], v[24:31], v[40:47], v[116:119], v235, v235 op_sel_hi:[0,0,0]
	s_waitcnt lgkmcnt(2)
	v_mfma_scale_f32_16x16x128_f8f6f4 v[112:115], v[16:23], v[48:55], v[112:115], v235, v235 op_sel_hi:[0,0,0]
	v_mfma_scale_f32_16x16x128_f8f6f4 v[108:111], v[24:31], v[48:55], v[108:111], v235, v235 op_sel_hi:[0,0,0]
	s_waitcnt lgkmcnt(0)
	v_mfma_scale_f32_16x16x128_f8f6f4 v[104:107], v[16:23], v[56:63], v[104:107], v235, v235 op_sel_hi:[0,0,0]
	v_mfma_scale_f32_16x16x128_f8f6f4 v[100:103], v[24:31], v[56:63], v[100:103], v235, v235 op_sel_hi:[0,0,0]
	s_setprio 0
	s_setprio 1
	v_mfma_scale_f32_16x16x128_f8f6f4 v[96:99], v[8:15], v[32:39], v[96:99], v235, v235 op_sel_hi:[0,0,0]
	v_mfma_scale_f32_16x16x128_f8f6f4 v[92:95], v[0:7], v[32:39], v[92:95], v235, v235 op_sel_hi:[0,0,0]
	v_mfma_scale_f32_16x16x128_f8f6f4 v[88:91], v[8:15], v[40:47], v[88:91], v235, v235 op_sel_hi:[0,0,0]
	v_mfma_scale_f32_16x16x128_f8f6f4 v[84:87], v[0:7], v[40:47], v[84:87], v235, v235 op_sel_hi:[0,0,0]
	v_mfma_scale_f32_16x16x128_f8f6f4 v[80:83], v[8:15], v[48:55], v[80:83], v235, v235 op_sel_hi:[0,0,0]
	v_mfma_scale_f32_16x16x128_f8f6f4 v[76:79], v[0:7], v[48:55], v[76:79], v235, v235 op_sel_hi:[0,0,0]
	v_mfma_scale_f32_16x16x128_f8f6f4 v[72:75], v[8:15], v[56:63], v[72:75], v235, v235 op_sel_hi:[0,0,0]
	v_mfma_scale_f32_16x16x128_f8f6f4 v[68:71], v[0:7], v[56:63], v[68:71], v235, v235 op_sel_hi:[0,0,0]
	s_setprio 0
	s_barrier
	s_andn2_b64 vcc, exec, s[20:21]
	s_cbranch_vccnz .LBB0_1371
	s_barrier

.LBB0_1452:
	s_add_i32 s33, s80, 0x180
	s_add_i32 s36, s81, 0x180
	s_waitcnt lgkmcnt(6)
	s_barrier
	s_setprio 1
	v_mfma_scale_f32_16x16x128_f8f6f4 v[128:131], v[24:31], v[56:63], 0, v235, v235 op_sel_hi:[0,0,0]
	v_mfma_scale_f32_16x16x128_f8f6f4 v[124:127], v[16:23], v[56:63], 0, v235, v235 op_sel_hi:[0,0,0]
	s_waitcnt lgkmcnt(4)
	v_mfma_scale_f32_16x16x128_f8f6f4 v[120:123], v[24:31], v[48:55], 0, v235, v235 op_sel_hi:[0,0,0]
	v_mfma_scale_f32_16x16x128_f8f6f4 v[116:119], v[16:23], v[48:55], 0, v235, v235 op_sel_hi:[0,0,0]
	s_waitcnt lgkmcnt(2)
	v_mfma_scale_f32_16x16x128_f8f6f4 v[112:115], v[24:31], v[40:47], 0, v235, v235 op_sel_hi:[0,0,0]
	v_mfma_scale_f32_16x16x128_f8f6f4 v[108:111], v[16:23], v[40:47], 0, v235, v235 op_sel_hi:[0,0,0]
	s_waitcnt lgkmcnt(0)
	v_mfma_scale_f32_16x16x128_f8f6f4 v[104:107], v[24:31], v[32:39], 0, v235, v235 op_sel_hi:[0,0,0]
	v_mfma_scale_f32_16x16x128_f8f6f4 v[100:103], v[16:23], v[32:39], 0, v235, v235 op_sel_hi:[0,0,0]
	s_setprio 0
	s_setprio 1
	v_mfma_scale_f32_16x16x128_f8f6f4 v[96:99], v[8:15], v[56:63], 0, v235, v235 op_sel_hi:[0,0,0]
	v_mfma_scale_f32_16x16x128_f8f6f4 v[92:95], v[0:7], v[56:63], 0, v235, v235 op_sel_hi:[0,0,0]
	v_mfma_scale_f32_16x16x128_f8f6f4 v[88:91], v[8:15], v[48:55], 0, v235, v235 op_sel_hi:[0,0,0]
	v_mfma_scale_f32_16x16x128_f8f6f4 v[84:87], v[0:7], v[48:55], 0, v235, v235 op_sel_hi:[0,0,0]
	v_mfma_scale_f32_16x16x128_f8f6f4 v[80:83], v[8:15], v[40:47], 0, v235, v235 op_sel_hi:[0,0,0]
	v_mfma_scale_f32_16x16x128_f8f6f4 v[76:79], v[0:7], v[40:47], 0, v235, v235 op_sel_hi:[0,0,0]
	v_mfma_scale_f32_16x16x128_f8f6f4 v[72:75], v[8:15], v[32:39], 0, v235, v235 op_sel_hi:[0,0,0]
	v_mfma_scale_f32_16x16x128_f8f6f4 v[68:71], v[0:7], v[32:39], 0, v235, v235 op_sel_hi:[0,0,0]
	s_setprio 0
	s_barrier
	ds_read_b128 v[16:19], v233 offset:0x8000
	ds_read_b128 v[20:23], v233 offset:0x8400
	ds_read_b128 v[24:27], v233 offset:0x8800
	ds_read_b128 v[28:31], v233 offset:0x8c00
	ds_read_b128 v[32:35], v232 offset:0x8000
	ds_read_b128 v[36:39], v232 offset:0x8400
	ds_read_b128 v[40:43], v232 offset:0x8800
	ds_read_b128 v[44:47], v232 offset:0x8c00
	ds_read_b128 v[48:51], v232 offset:0x9000
	ds_read_b128 v[52:55], v232 offset:0x9400
	ds_read_b128 v[56:59], v232 offset:0x9800
	ds_read_b128 v[60:63], v232 offset:0x9c00
	ds_read_b128 v[8:11], v233 offset:0xc000
	ds_read_b128 v[12:15], v233 offset:0xc400
	ds_read_b128 v[0:3], v233 offset:0xc800
	ds_read_b128 v[4:7], v233 offset:0xcc00
	s_mov_b32 m0, s62
	s_add_i32 s10, s80, 0x10100
	buffer_load_dwordx4 v230, s[4:7], s10 offen lds
	s_add_i32 s10, s80, 0x18100
	s_mov_b32 m0, s63
	s_nop 0
	buffer_load_dwordx4 v230, s[4:7], s10 offen lds
	s_waitcnt vmcnt(8)
	s_waitcnt lgkmcnt(8)
	s_barrier
	s_setprio 1
	v_mfma_scale_f32_16x16x128_f8f6f4 v[192:195], v[16:23], v[32:39], v[192:195], v235, v235 op_sel_hi:[0,0,0]
	v_mfma_scale_f32_16x16x128_f8f6f4 v[188:191], v[24:31], v[32:39], v[188:191], v235, v235 op_sel_hi:[0,0,0]
	v_mfma_scale_f32_16x16x128_f8f6f4 v[184:187], v[16:23], v[40:47], v[184:187], v235, v235 op_sel_hi:[0,0,0]
	v_mfma_scale_f32_16x16x128_f8f6f4 v[180:183], v[24:31], v[40:47], v[180:183], v235, v235 op_sel_hi:[0,0,0]
	s_waitcnt lgkmcnt(6)
	v_mfma_scale_f32_16x16x128_f8f6f4 v[176:179], v[16:23], v[48:55], v[176:179], v235, v235 op_sel_hi:[0,0,0]
	v_mfma_scale_f32_16x16x128_f8f6f4 v[172:175], v[24:31], v[48:55], v[172:175], v235, v235 op_sel_hi:[0,0,0]
	s_waitcnt lgkmcnt(4)
	v_mfma_scale_f32_16x16x128_f8f6f4 v[168:171], v[16:23], v[56:63], v[168:171], v235, v235 op_sel_hi:[0,0,0]
	v_mfma_scale_f32_16x16x128_f8f6f4 v[164:167], v[24:31], v[56:63], v[164:167], v235, v235 op_sel_hi:[0,0,0]
	s_setprio 0
	s_setprio 1
	s_waitcnt lgkmcnt(2)
	v_mfma_scale_f32_16x16x128_f8f6f4 v[160:163], v[8:15], v[32:39], v[160:163], v235, v235 op_sel_hi:[0,0,0]
	s_waitcnt lgkmcnt(0)
	v_mfma_scale_f32_16x16x128_f8f6f4 v[156:159], v[0:7], v[32:39], v[156:159], v235, v235 op_sel_hi:[0,0,0]
	v_mfma_scale_f32_16x16x128_f8f6f4 v[152:155], v[8:15], v[40:47], v[152:155], v235, v235 op_sel_hi:[0,0,0]
	v_mfma_scale_f32_16x16x128_f8f6f4 v[148:151], v[0:7], v[40:47], v[148:151], v235, v235 op_sel_hi:[0,0,0]
	v_mfma_scale_f32_16x16x128_f8f6f4 v[144:147], v[8:15], v[48:55], v[144:147], v235, v235 op_sel_hi:[0,0,0]
	v_mfma_scale_f32_16x16x128_f8f6f4 v[140:143], v[0:7], v[48:55], v[140:143], v235, v235 op_sel_hi:[0,0,0]
	v_mfma_scale_f32_16x16x128_f8f6f4 v[136:139], v[8:15], v[56:63], v[136:139], v235, v235 op_sel_hi:[0,0,0]
	v_mfma_scale_f32_16x16x128_f8f6f4 v[132:135], v[0:7], v[56:63], v[132:135], v235, v235 op_sel_hi:[0,0,0]
	s_setprio 0
	s_barrier
	ds_read_b128 v[32:35], v232 offset:0xc000
	ds_read_b128 v[36:39], v232 offset:0xc400
	ds_read_b128 v[40:43], v232 offset:0xc800
	ds_read_b128 v[44:47], v232 offset:0xcc00
	ds_read_b128 v[48:51], v232 offset:0xd000
	ds_read_b128 v[52:55], v232 offset:0xd400
	ds_read_b128 v[56:59], v232 offset:0xd800
	ds_read_b128 v[60:63], v232 offset:0xdc00
	s_mov_b32 m0, s64
	s_mov_b32 s10, s6
	s_mov_b32 s11, s7
	buffer_load_dwordx4 v231, s[8:11], s36 offen lds
	s_add_i32 s36, s81, 0x10180
	s_mov_b32 m0, s65
	s_nop 0
	buffer_load_dwordx4 v231, s[8:11], s36 offen lds
	s_add_i32 s36, s81, 0x1180
	s_mov_b32 m0, s70
	s_nop 0
	buffer_load_dwordx4 v231, s[8:11], s36 offen lds
	s_add_i32 s36, s81, 0x11180
	s_mov_b32 m0, s71
	s_nop 0
	buffer_load_dwordx4 v231, s[8:11], s36 offen lds
	s_mov_b32 m0, s68
	s_nop 0
	buffer_load_dwordx4 v230, s[4:7], s33 offen lds
	s_add_i32 s33, s80, 0x8180
	s_mov_b32 m0, s69
	s_nop 0
	buffer_load_dwordx4 v230, s[4:7], s33 offen lds
	s_waitcnt vmcnt(8)
	s_waitcnt lgkmcnt(6)
	s_barrier
	s_setprio 1
	v_mfma_scale_f32_16x16x128_f8f6f4 v[128:131], v[16:23], v[32:39], v[128:131], v235, v235 op_sel_hi:[0,0,0]
	v_mfma_scale_f32_16x16x128_f8f6f4 v[124:127], v[24:31], v[32:39], v[124:127], v235, v235 op_sel_hi:[0,0,0]
	s_waitcnt lgkmcnt(4)
	v_mfma_scale_f32_16x16x128_f8f6f4 v[120:123], v[16:23], v[40:47], v[120:123], v235, v235 op_sel_hi:[0,0,0]
	v_mfma_scale_f32_16x16x128_f8f6f4 v[116:119], v[24:31], v[40:47], v[116:119], v235, v235 op_sel_hi:[0,0,0]
	s_waitcnt lgkmcnt(2)
	v_mfma_scale_f32_16x16x128_f8f6f4 v[112:115], v[16:23], v[48:55], v[112:115], v235, v235 op_sel_hi:[0,0,0]
	v_mfma_scale_f32_16x16x128_f8f6f4 v[108:111], v[24:31], v[48:55], v[108:111], v235, v235 op_sel_hi:[0,0,0]
	s_waitcnt lgkmcnt(0)
	v_mfma_scale_f32_16x16x128_f8f6f4 v[104:107], v[16:23], v[56:63], v[104:107], v235, v235 op_sel_hi:[0,0,0]
	v_mfma_scale_f32_16x16x128_f8f6f4 v[100:103], v[24:31], v[56:63], v[100:103], v235, v235 op_sel_hi:[0,0,0]
	s_setprio 0
	s_setprio 1
	v_mfma_scale_f32_16x16x128_f8f6f4 v[96:99], v[8:15], v[32:39], v[96:99], v235, v235 op_sel_hi:[0,0,0]
	v_mfma_scale_f32_16x16x128_f8f6f4 v[92:95], v[0:7], v[32:39], v[92:95], v235, v235 op_sel_hi:[0,0,0]
	v_mfma_scale_f32_16x16x128_f8f6f4 v[88:91], v[8:15], v[40:47], v[88:91], v235, v235 op_sel_hi:[0,0,0]
	v_mfma_scale_f32_16x16x128_f8f6f4 v[84:87], v[0:7], v[40:47], v[84:87], v235, v235 op_sel_hi:[0,0,0]
	v_mfma_scale_f32_16x16x128_f8f6f4 v[80:83], v[8:15], v[48:55], v[80:83], v235, v235 op_sel_hi:[0,0,0]
	v_mfma_scale_f32_16x16x128_f8f6f4 v[76:79], v[0:7], v[48:55], v[76:79], v235, v235 op_sel_hi:[0,0,0]
	v_mfma_scale_f32_16x16x128_f8f6f4 v[72:75], v[8:15], v[56:63], v[72:75], v235, v235 op_sel_hi:[0,0,0]
	v_mfma_scale_f32_16x16x128_f8f6f4 v[68:71], v[0:7], v[56:63], v[68:71], v235, v235 op_sel_hi:[0,0,0]
	s_setprio 0
	s_barrier
	ds_read_b128 v[16:19], v233 offset:0
	ds_read_b128 v[20:23], v233 offset:0x400
	ds_read_b128 v[24:27], v233 offset:0x800
	ds_read_b128 v[28:31], v233 offset:0xc00
	ds_read_b128 v[32:35], v232 offset:0
	ds_read_b128 v[36:39], v232 offset:0x400
	ds_read_b128 v[40:43], v232 offset:0x800
	ds_read_b128 v[44:47], v232 offset:0xc00
	ds_read_b128 v[48:51], v232 offset:0x1000
	ds_read_b128 v[52:55], v232 offset:0x1400
	ds_read_b128 v[56:59], v232 offset:0x1800
	ds_read_b128 v[60:63], v232 offset:0x1c00
	ds_read_b128 v[8:11], v233 offset:0x4000
	ds_read_b128 v[12:15], v233 offset:0x4400
	ds_read_b128 v[0:3], v233 offset:0x4800
	ds_read_b128 v[4:7], v233 offset:0x4c00
	s_add_i32 s33, s43, 0x80
	s_mov_b32 m0, s74
	s_add_i32 s36, s80, 0x10180
	buffer_load_dwordx4 v230, s[4:7], s36 offen lds
	s_add_i32 s36, s80, 0x18180
	s_mov_b32 m0, s76
	s_nop 0
	buffer_load_dwordx4 v230, s[4:7], s36 offen lds
	s_waitcnt vmcnt(8)
	s_waitcnt lgkmcnt(8)
	s_barrier
	s_setprio 1
	v_mfma_scale_f32_16x16x128_f8f6f4 v[192:195], v[16:23], v[32:39], v[192:195], v235, v235 op_sel_hi:[0,0,0]
	v_mfma_scale_f32_16x16x128_f8f6f4 v[188:191], v[24:31], v[32:39], v[188:191], v235, v235 op_sel_hi:[0,0,0]
	v_mfma_scale_f32_16x16x128_f8f6f4 v[184:187], v[16:23], v[40:47], v[184:187], v235, v235 op_sel_hi:[0,0,0]
	v_mfma_scale_f32_16x16x128_f8f6f4 v[180:183], v[24:31], v[40:47], v[180:183], v235, v235 op_sel_hi:[0,0,0]
	s_waitcnt lgkmcnt(6)
	v_mfma_scale_f32_16x16x128_f8f6f4 v[176:179], v[16:23], v[48:55], v[176:179], v235, v235 op_sel_hi:[0,0,0]
	v_mfma_scale_f32_16x16x128_f8f6f4 v[172:175], v[24:31], v[48:55], v[172:175], v235, v235 op_sel_hi:[0,0,0]
	s_waitcnt lgkmcnt(4)
	v_mfma_scale_f32_16x16x128_f8f6f4 v[168:171], v[16:23], v[56:63], v[168:171], v235, v235 op_sel_hi:[0,0,0]
	v_mfma_scale_f32_16x16x128_f8f6f4 v[164:167], v[24:31], v[56:63], v[164:167], v235, v235 op_sel_hi:[0,0,0]
	s_setprio 0
	s_setprio 1
	s_waitcnt lgkmcnt(2)
	v_mfma_scale_f32_16x16x128_f8f6f4 v[160:163], v[8:15], v[32:39], v[160:163], v235, v235 op_sel_hi:[0,0,0]
	s_waitcnt lgkmcnt(0)
	v_mfma_scale_f32_16x16x128_f8f6f4 v[156:159], v[0:7], v[32:39], v[156:159], v235, v235 op_sel_hi:[0,0,0]
	v_mfma_scale_f32_16x16x128_f8f6f4 v[152:155], v[8:15], v[40:47], v[152:155], v235, v235 op_sel_hi:[0,0,0]
	v_mfma_scale_f32_16x16x128_f8f6f4 v[148:151], v[0:7], v[40:47], v[148:151], v235, v235 op_sel_hi:[0,0,0]
	v_mfma_scale_f32_16x16x128_f8f6f4 v[144:147], v[8:15], v[48:55], v[144:147], v235, v235 op_sel_hi:[0,0,0]
	v_mfma_scale_f32_16x16x128_f8f6f4 v[140:143], v[0:7], v[48:55], v[140:143], v235, v235 op_sel_hi:[0,0,0]
	v_mfma_scale_f32_16x16x128_f8f6f4 v[136:139], v[8:15], v[56:63], v[136:139], v235, v235 op_sel_hi:[0,0,0]
	v_mfma_scale_f32_16x16x128_f8f6f4 v[132:135], v[0:7], v[56:63], v[132:135], v235, v235 op_sel_hi:[0,0,0]
	s_setprio 0
	s_barrier
	ds_read_b128 v[32:35], v232 offset:0x4000
	ds_read_b128 v[36:39], v232 offset:0x4400
	ds_read_b128 v[40:43], v232 offset:0x4800
	ds_read_b128 v[44:47], v232 offset:0x4c00
	ds_read_b128 v[48:51], v232 offset:0x5000
	ds_read_b128 v[52:55], v232 offset:0x5400
	ds_read_b128 v[56:59], v232 offset:0x5800
	ds_read_b128 v[60:63], v232 offset:0x5c00
	s_mov_b32 m0, s46
	s_nop 0
	buffer_load_dwordx4 v231, s[8:11], s78 offen lds
	s_add_i32 s36, s78, 0x10000
	s_mov_b32 m0, s47
	s_nop 0
	buffer_load_dwordx4 v231, s[8:11], s36 offen lds
	s_add_i32 s36, s78, 0x1000
	s_mov_b32 m0, s49
	s_nop 0
	buffer_load_dwordx4 v231, s[8:11], s36 offen lds
	s_add_i32 s36, s78, 0x11000
	s_mov_b32 m0, s50
	s_nop 0
	buffer_load_dwordx4 v231, s[8:11], s36 offen lds
	s_mov_b32 m0, s48
	s_add_i32 s36, s43, 0x8000
	buffer_load_dwordx4 v230, s[4:7], s43 offen lds
	s_mov_b32 m0, s51
	s_nop 0
	buffer_load_dwordx4 v230, s[4:7], s36 offen lds
	s_waitcnt vmcnt(8)
	s_waitcnt lgkmcnt(6)
	s_barrier
	s_setprio 1
	v_mfma_scale_f32_16x16x128_f8f6f4 v[128:131], v[16:23], v[32:39], v[128:131], v235, v235 op_sel_hi:[0,0,0]
	v_mfma_scale_f32_16x16x128_f8f6f4 v[124:127], v[24:31], v[32:39], v[124:127], v235, v235 op_sel_hi:[0,0,0]
	s_waitcnt lgkmcnt(4)
	v_mfma_scale_f32_16x16x128_f8f6f4 v[120:123], v[16:23], v[40:47], v[120:123], v235, v235 op_sel_hi:[0,0,0]
	v_mfma_scale_f32_16x16x128_f8f6f4 v[116:119], v[24:31], v[40:47], v[116:119], v235, v235 op_sel_hi:[0,0,0]
	s_waitcnt lgkmcnt(2)
	v_mfma_scale_f32_16x16x128_f8f6f4 v[112:115], v[16:23], v[48:55], v[112:115], v235, v235 op_sel_hi:[0,0,0]
	v_mfma_scale_f32_16x16x128_f8f6f4 v[108:111], v[24:31], v[48:55], v[108:111], v235, v235 op_sel_hi:[0,0,0]
	s_waitcnt lgkmcnt(0)
	v_mfma_scale_f32_16x16x128_f8f6f4 v[104:107], v[16:23], v[56:63], v[104:107], v235, v235 op_sel_hi:[0,0,0]
	v_mfma_scale_f32_16x16x128_f8f6f4 v[100:103], v[24:31], v[56:63], v[100:103], v235, v235 op_sel_hi:[0,0,0]
	s_setprio 0
	s_setprio 1
	v_mfma_scale_f32_16x16x128_f8f6f4 v[96:99], v[8:15], v[32:39], v[96:99], v235, v235 op_sel_hi:[0,0,0]
	v_mfma_scale_f32_16x16x128_f8f6f4 v[92:95], v[0:7], v[32:39], v[92:95], v235, v235 op_sel_hi:[0,0,0]
	v_mfma_scale_f32_16x16x128_f8f6f4 v[88:91], v[8:15], v[40:47], v[88:91], v235, v235 op_sel_hi:[0,0,0]
	v_mfma_scale_f32_16x16x128_f8f6f4 v[84:87], v[0:7], v[40:47], v[84:87], v235, v235 op_sel_hi:[0,0,0]
	v_mfma_scale_f32_16x16x128_f8f6f4 v[80:83], v[8:15], v[48:55], v[80:83], v235, v235 op_sel_hi:[0,0,0]
	v_mfma_scale_f32_16x16x128_f8f6f4 v[76:79], v[0:7], v[48:55], v[76:79], v235, v235 op_sel_hi:[0,0,0]
	v_mfma_scale_f32_16x16x128_f8f6f4 v[72:75], v[8:15], v[56:63], v[72:75], v235, v235 op_sel_hi:[0,0,0]
	v_mfma_scale_f32_16x16x128_f8f6f4 v[68:71], v[0:7], v[56:63], v[68:71], v235, v235 op_sel_hi:[0,0,0]
	s_setprio 0
	s_barrier
	ds_read_b128 v[16:19], v233 offset:0x8000
	ds_read_b128 v[20:23], v233 offset:0x8400
	ds_read_b128 v[24:27], v233 offset:0x8800
	ds_read_b128 v[28:31], v233 offset:0x8c00
	ds_read_b128 v[32:35], v232 offset:0x8000
	ds_read_b128 v[36:39], v232 offset:0x8400
	ds_read_b128 v[40:43], v232 offset:0x8800
	ds_read_b128 v[44:47], v232 offset:0x8c00
	ds_read_b128 v[48:51], v232 offset:0x9000
	ds_read_b128 v[52:55], v232 offset:0x9400
	ds_read_b128 v[56:59], v232 offset:0x9800
	ds_read_b128 v[60:63], v232 offset:0x9c00
	ds_read_b128 v[8:11], v233 offset:0xc000
	ds_read_b128 v[12:15], v233 offset:0xc400
	ds_read_b128 v[0:3], v233 offset:0xc800
	ds_read_b128 v[4:7], v233 offset:0xcc00
	s_mov_b32 m0, s62
	s_add_i32 s36, s43, 0x10000
	buffer_load_dwordx4 v230, s[4:7], s36 offen lds
	s_add_i32 s36, s43, 0x18000
	s_mov_b32 m0, s63
	s_nop 0
	buffer_load_dwordx4 v230, s[4:7], s36 offen lds
	s_waitcnt vmcnt(8)
	s_waitcnt lgkmcnt(8)
	s_barrier
	s_setprio 1
	v_mfma_scale_f32_16x16x128_f8f6f4 v[192:195], v[16:23], v[32:39], v[192:195], v235, v235 op_sel_hi:[0,0,0]
	v_mfma_scale_f32_16x16x128_f8f6f4 v[188:191], v[24:31], v[32:39], v[188:191], v235, v235 op_sel_hi:[0,0,0]
	v_mfma_scale_f32_16x16x128_f8f6f4 v[184:187], v[16:23], v[40:47], v[184:187], v235, v235 op_sel_hi:[0,0,0]
	v_mfma_scale_f32_16x16x128_f8f6f4 v[180:183], v[24:31], v[40:47], v[180:183], v235, v235 op_sel_hi:[0,0,0]
	s_waitcnt lgkmcnt(6)
	v_mfma_scale_f32_16x16x128_f8f6f4 v[176:179], v[16:23], v[48:55], v[176:179], v235, v235 op_sel_hi:[0,0,0]
	v_mfma_scale_f32_16x16x128_f8f6f4 v[172:175], v[24:31], v[48:55], v[172:175], v235, v235 op_sel_hi:[0,0,0]
	s_waitcnt lgkmcnt(4)
	v_mfma_scale_f32_16x16x128_f8f6f4 v[168:171], v[16:23], v[56:63], v[168:171], v235, v235 op_sel_hi:[0,0,0]
	v_mfma_scale_f32_16x16x128_f8f6f4 v[164:167], v[24:31], v[56:63], v[164:167], v235, v235 op_sel_hi:[0,0,0]
	s_setprio 0
	s_setprio 1
	s_waitcnt lgkmcnt(2)
	v_mfma_scale_f32_16x16x128_f8f6f4 v[160:163], v[8:15], v[32:39], v[160:163], v235, v235 op_sel_hi:[0,0,0]
	s_waitcnt lgkmcnt(0)
	v_mfma_scale_f32_16x16x128_f8f6f4 v[156:159], v[0:7], v[32:39], v[156:159], v235, v235 op_sel_hi:[0,0,0]
	v_mfma_scale_f32_16x16x128_f8f6f4 v[152:155], v[8:15], v[40:47], v[152:155], v235, v235 op_sel_hi:[0,0,0]
	v_mfma_scale_f32_16x16x128_f8f6f4 v[148:151], v[0:7], v[40:47], v[148:151], v235, v235 op_sel_hi:[0,0,0]
	v_mfma_scale_f32_16x16x128_f8f6f4 v[144:147], v[8:15], v[48:55], v[144:147], v235, v235 op_sel_hi:[0,0,0]
	v_mfma_scale_f32_16x16x128_f8f6f4 v[140:143], v[0:7], v[48:55], v[140:143], v235, v235 op_sel_hi:[0,0,0]
	v_mfma_scale_f32_16x16x128_f8f6f4 v[136:139], v[8:15], v[56:63], v[136:139], v235, v235 op_sel_hi:[0,0,0]
	v_mfma_scale_f32_16x16x128_f8f6f4 v[132:135], v[0:7], v[56:63], v[132:135], v235, v235 op_sel_hi:[0,0,0]
	s_setprio 0
	s_barrier
	ds_read_b128 v[32:35], v232 offset:0xc000
	ds_read_b128 v[36:39], v232 offset:0xc400
	ds_read_b128 v[40:43], v232 offset:0xc800
	ds_read_b128 v[44:47], v232 offset:0xcc00
	ds_read_b128 v[48:51], v232 offset:0xd000
	ds_read_b128 v[52:55], v232 offset:0xd400
	ds_read_b128 v[56:59], v232 offset:0xd800
	ds_read_b128 v[60:63], v232 offset:0xdc00
	s_mov_b32 m0, s64
	s_add_i32 s36, s78, 0x80
	buffer_load_dwordx4 v231, s[8:11], s36 offen lds
	s_add_i32 s36, s78, 0x10080
	s_mov_b32 m0, s65
	s_nop 0
	buffer_load_dwordx4 v231, s[8:11], s36 offen lds
	s_add_i32 s36, s78, 0x1080
	s_mov_b32 m0, s70
	s_nop 0
	buffer_load_dwordx4 v231, s[8:11], s36 offen lds
	s_add_i32 s36, s78, 0x11080
	s_mov_b32 m0, s71
	s_nop 0
	buffer_load_dwordx4 v231, s[8:11], s36 offen lds
	s_mov_b32 m0, s68
	s_add_i32 s10, s43, 0x8080
	buffer_load_dwordx4 v230, s[4:7], s33 offen lds
	s_mov_b32 m0, s69
	s_nop 0
	buffer_load_dwordx4 v230, s[4:7], s10 offen lds
	s_waitcnt vmcnt(8)
	s_waitcnt lgkmcnt(6)
	s_barrier
	s_setprio 1
	v_mfma_scale_f32_16x16x128_f8f6f4 v[128:131], v[16:23], v[32:39], v[128:131], v235, v235 op_sel_hi:[0,0,0]
	v_mfma_scale_f32_16x16x128_f8f6f4 v[124:127], v[24:31], v[32:39], v[124:127], v235, v235 op_sel_hi:[0,0,0]
	s_waitcnt lgkmcnt(4)
	v_mfma_scale_f32_16x16x128_f8f6f4 v[120:123], v[16:23], v[40:47], v[120:123], v235, v235 op_sel_hi:[0,0,0]
	v_mfma_scale_f32_16x16x128_f8f6f4 v[116:119], v[24:31], v[40:47], v[116:119], v235, v235 op_sel_hi:[0,0,0]
	s_waitcnt lgkmcnt(2)
	v_mfma_scale_f32_16x16x128_f8f6f4 v[112:115], v[16:23], v[48:55], v[112:115], v235, v235 op_sel_hi:[0,0,0]
	v_mfma_scale_f32_16x16x128_f8f6f4 v[108:111], v[24:31], v[48:55], v[108:111], v235, v235 op_sel_hi:[0,0,0]
	s_waitcnt lgkmcnt(0)
	v_mfma_scale_f32_16x16x128_f8f6f4 v[104:107], v[16:23], v[56:63], v[104:107], v235, v235 op_sel_hi:[0,0,0]
	v_mfma_scale_f32_16x16x128_f8f6f4 v[100:103], v[24:31], v[56:63], v[100:103], v235, v235 op_sel_hi:[0,0,0]
	s_setprio 0
	s_setprio 1
	v_mfma_scale_f32_16x16x128_f8f6f4 v[96:99], v[8:15], v[32:39], v[96:99], v235, v235 op_sel_hi:[0,0,0]
	v_mfma_scale_f32_16x16x128_f8f6f4 v[92:95], v[0:7], v[32:39], v[92:95], v235, v235 op_sel_hi:[0,0,0]
	v_mfma_scale_f32_16x16x128_f8f6f4 v[88:91], v[8:15], v[40:47], v[88:91], v235, v235 op_sel_hi:[0,0,0]
	v_mfma_scale_f32_16x16x128_f8f6f4 v[84:87], v[0:7], v[40:47], v[84:87], v235, v235 op_sel_hi:[0,0,0]
	v_mfma_scale_f32_16x16x128_f8f6f4 v[80:83], v[8:15], v[48:55], v[80:83], v235, v235 op_sel_hi:[0,0,0]
	v_mfma_scale_f32_16x16x128_f8f6f4 v[76:79], v[0:7], v[48:55], v[76:79], v235, v235 op_sel_hi:[0,0,0]
	v_mfma_scale_f32_16x16x128_f8f6f4 v[72:75], v[8:15], v[56:63], v[72:75], v235, v235 op_sel_hi:[0,0,0]
	v_mfma_scale_f32_16x16x128_f8f6f4 v[68:71], v[0:7], v[56:63], v[68:71], v235, v235 op_sel_hi:[0,0,0]
	s_setprio 0
	s_barrier
	s_andn2_b64 vcc, exec, s[20:21]
	s_cbranch_vccnz .LBB0_1454
	s_barrier
